# unfused GEMM unit end: the leading half starts its epilogue during the trailing half's last MFMA segment; its alignment barrier sits after the 4th store group (E1-even, E1-odd, C6), on top of v056
# baseline (speedup 1.0000x reference)
.LBB0_417:
	s_add_u32 s28, s6, 0xfffc0080
	s_addc_u32 s29, s7, -1
	s_add_i32 s43, 0, 0x10000
	s_cmp_eq_u32 s42, 12
	s_cselect_b32 s31, s5, s29
	s_cselect_b32 s30, s8, s28
	s_cselect_b32 s29, s9, s33
	s_cselect_b32 s28, s21, s23
	s_add_i32 s63, 0, 0x14000
	ds_read_b128 v[130:133], v165
	ds_read_b128 v[134:137], v165 offset:1024
	ds_read_b128 v[138:141], v165 offset:2048
	ds_read_b128 v[142:145], v165 offset:3072
	ds_read_b128 v[146:149], v165 offset:16384
	ds_read_b128 v[150:153], v165 offset:17408
	ds_read_b128 v[154:157], v165 offset:18432
	ds_read_b128 v[168:171], v165 offset:19456
	s_add_i32 m0, s45, 0xc000
	ds_read_b128 v[172:175], v188
	ds_read_b128 v[176:179], v188 offset:1024
	ds_read_b128 v[180:183], v188 offset:2048
	ds_read_b128 v[190:193], v188 offset:3072
	ds_read_b128 v[194:197], v188 offset:4096
	ds_read_b128 v[198:201], v188 offset:5120
	ds_read_b128 v[202:205], v188 offset:6144
	global_load_lds_dwordx4 v166, s[6:7]
	s_add_i32 m0, s45, 0xe000
	ds_read_b128 v[206:209], v188 offset:7168
	global_load_lds_dwordx4 v164, s[6:7]
	s_waitcnt vmcnt(8) lgkmcnt(0)
	s_barrier
	v_mfma_f32_16x16x32_bf16 v[126:129], v[130:133], v[172:175], v[126:129]
	v_mfma_f32_16x16x32_bf16 v[122:125], v[138:141], v[172:175], v[122:125]
	v_mfma_f32_16x16x32_bf16 v[114:117], v[130:133], v[180:183], v[114:117]
	v_mfma_f32_16x16x32_bf16 v[106:109], v[138:141], v[180:183], v[106:109]
	v_mfma_f32_16x16x32_bf16 v[98:101], v[130:133], v[194:197], v[98:101]
	v_mfma_f32_16x16x32_bf16 v[90:93], v[138:141], v[194:197], v[90:93]
	v_mfma_f32_16x16x32_bf16 v[82:85], v[130:133], v[202:205], v[82:85]
	v_mfma_f32_16x16x32_bf16 v[74:77], v[138:141], v[202:205], v[74:77]
	v_mfma_f32_16x16x32_bf16 v[126:129], v[134:137], v[176:179], v[126:129]
	v_mfma_f32_16x16x32_bf16 v[122:125], v[142:145], v[176:179], v[122:125]
	v_mfma_f32_16x16x32_bf16 v[114:117], v[134:137], v[190:193], v[114:117]
	v_mfma_f32_16x16x32_bf16 v[106:109], v[142:145], v[190:193], v[106:109]
	v_mfma_f32_16x16x32_bf16 v[98:101], v[134:137], v[198:201], v[98:101]
	v_mfma_f32_16x16x32_bf16 v[90:93], v[142:145], v[198:201], v[90:93]
	v_mfma_f32_16x16x32_bf16 v[82:85], v[134:137], v[206:209], v[82:85]
	v_mfma_f32_16x16x32_bf16 v[74:77], v[142:145], v[206:209], v[74:77]
	v_mfma_f32_16x16x32_bf16 v[118:121], v[146:149], v[172:175], v[118:121]
	v_mfma_f32_16x16x32_bf16 v[110:113], v[154:157], v[172:175], v[110:113]
	v_mfma_f32_16x16x32_bf16 v[102:105], v[146:149], v[180:183], v[102:105]
	v_mfma_f32_16x16x32_bf16 v[94:97], v[154:157], v[180:183], v[94:97]
	v_mfma_f32_16x16x32_bf16 v[86:89], v[146:149], v[194:197], v[86:89]
	v_mfma_f32_16x16x32_bf16 v[78:81], v[154:157], v[194:197], v[78:81]
	v_mfma_f32_16x16x32_bf16 v[70:73], v[146:149], v[202:205], v[70:73]
	v_mfma_f32_16x16x32_bf16 v[66:69], v[154:157], v[202:205], v[66:69]
	v_mfma_f32_16x16x32_bf16 v[118:121], v[150:153], v[176:179], v[118:121]
	v_mfma_f32_16x16x32_bf16 v[110:113], v[168:171], v[176:179], v[110:113]
	v_mfma_f32_16x16x32_bf16 v[102:105], v[150:153], v[190:193], v[102:105]
	v_mfma_f32_16x16x32_bf16 v[94:97], v[168:171], v[190:193], v[94:97]
	v_mfma_f32_16x16x32_bf16 v[86:89], v[150:153], v[198:201], v[86:89]
	v_mfma_f32_16x16x32_bf16 v[78:81], v[168:171], v[198:201], v[78:81]
	v_mfma_f32_16x16x32_bf16 v[70:73], v[150:153], v[206:209], v[70:73]
	v_mfma_f32_16x16x32_bf16 v[66:69], v[168:171], v[206:209], v[66:69]
	s_barrier
	s_add_i32 s43, s43, s44
	v_lshl_add_u64 v[216:217], s[28:29], 0, v[0:1]
	s_mov_b32 m0, s43
	ds_read_b128 v[172:175], v188 offset:16384
	ds_read_b128 v[176:179], v188 offset:17408
	ds_read_b128 v[180:183], v188 offset:18432
	ds_read_b128 v[190:193], v188 offset:19456
	ds_read_b128 v[194:197], v188 offset:20480
	ds_read_b128 v[198:201], v188 offset:21504
	ds_read_b128 v[202:205], v188 offset:22528
	ds_read_b128 v[206:209], v188 offset:23552
	global_load_lds_dwordx4 v0, s[28:29]
	s_add_i32 m0, s43, 0x2000
	s_add_u32 s58, s28, 0x40000
	v_lshl_add_u64 v[218:219], s[28:29], 0, v[158:159]
	s_addc_u32 s59, s29, 0
	s_add_i32 s43, s63, s44
	global_load_lds_dwordx4 v158, s[28:29]
	s_mov_b32 m0, s43
	v_lshl_add_u64 v[222:223], s[30:31], 0, v[160:161]
	global_load_lds_dwordx4 v0, s[58:59]
	s_add_i32 m0, s43, 0x2000
	s_nop 0
	global_load_lds_dwordx4 v158, s[58:59]
	s_mov_b32 m0, s45
	v_lshl_add_u64 v[220:221], s[30:31], 0, v[162:163]
	global_load_lds_dwordx4 v162, s[30:31]
	s_mov_b32 m0, s46
	s_nop 0
	global_load_lds_dwordx4 v160, s[30:31]
	s_waitcnt vmcnt(8) lgkmcnt(0)
	s_barrier
	v_mfma_f32_16x16x32_bf16 v[62:65], v[130:133], v[172:175], v[62:65]
	v_mfma_f32_16x16x32_bf16 v[58:61], v[138:141], v[172:175], v[58:61]
	v_mfma_f32_16x16x32_bf16 v[50:53], v[130:133], v[180:183], v[50:53]
	v_mfma_f32_16x16x32_bf16 v[42:45], v[138:141], v[180:183], v[42:45]
	v_mfma_f32_16x16x32_bf16 v[34:37], v[130:133], v[194:197], v[34:37]
	v_mfma_f32_16x16x32_bf16 v[26:29], v[138:141], v[194:197], v[26:29]
	v_mfma_f32_16x16x32_bf16 v[18:21], v[130:133], v[202:205], v[18:21]
	v_mfma_f32_16x16x32_bf16 v[10:13], v[138:141], v[202:205], v[10:13]
	v_mfma_f32_16x16x32_bf16 v[62:65], v[134:137], v[176:179], v[62:65]
	v_mfma_f32_16x16x32_bf16 v[58:61], v[142:145], v[176:179], v[58:61]
	v_mfma_f32_16x16x32_bf16 v[50:53], v[134:137], v[190:193], v[50:53]
	v_mfma_f32_16x16x32_bf16 v[42:45], v[142:145], v[190:193], v[42:45]
	v_mfma_f32_16x16x32_bf16 v[34:37], v[134:137], v[198:201], v[34:37]
	v_mfma_f32_16x16x32_bf16 v[26:29], v[142:145], v[198:201], v[26:29]
	v_mfma_f32_16x16x32_bf16 v[18:21], v[134:137], v[206:209], v[18:21]
	v_mfma_f32_16x16x32_bf16 v[10:13], v[142:145], v[206:209], v[10:13]
	v_mfma_f32_16x16x32_bf16 v[54:57], v[146:149], v[172:175], v[54:57]
	v_mfma_f32_16x16x32_bf16 v[46:49], v[154:157], v[172:175], v[46:49]
	v_mfma_f32_16x16x32_bf16 v[38:41], v[146:149], v[180:183], v[38:41]
	v_mfma_f32_16x16x32_bf16 v[30:33], v[154:157], v[180:183], v[30:33]
	v_mfma_f32_16x16x32_bf16 v[22:25], v[146:149], v[194:197], v[22:25]
	v_mfma_f32_16x16x32_bf16 v[14:17], v[154:157], v[194:197], v[14:17]
	v_mfma_f32_16x16x32_bf16 v[6:9], v[146:149], v[202:205], v[6:9]
	v_mfma_f32_16x16x32_bf16 v[2:5], v[154:157], v[202:205], v[2:5]
	v_mfma_f32_16x16x32_bf16 v[54:57], v[150:153], v[176:179], v[54:57]
	v_mfma_f32_16x16x32_bf16 v[46:49], v[168:171], v[176:179], v[46:49]
	v_mfma_f32_16x16x32_bf16 v[38:41], v[150:153], v[190:193], v[38:41]
	v_mfma_f32_16x16x32_bf16 v[30:33], v[168:171], v[190:193], v[30:33]
	v_mfma_f32_16x16x32_bf16 v[22:25], v[150:153], v[198:201], v[22:25]
	v_mfma_f32_16x16x32_bf16 v[14:17], v[168:171], v[198:201], v[14:17]
	v_mfma_f32_16x16x32_bf16 v[6:9], v[150:153], v[206:209], v[6:9]
	v_mfma_f32_16x16x32_bf16 v[2:5], v[168:171], v[206:209], v[2:5]
	s_barrier
	s_add_i32 s43, 0, 0x18000
	s_add_i32 s58, 0, 0x1c000
	ds_read_b128 v[130:133], v165 offset:32768
	ds_read_b128 v[134:137], v165 offset:33792
	ds_read_b128 v[138:141], v165 offset:34816
	ds_read_b128 v[142:145], v165 offset:35840
	ds_read_b128 v[146:149], v165 offset:49152
	ds_read_b128 v[150:153], v165 offset:50176
	ds_read_b128 v[154:157], v165 offset:51200
	ds_read_b128 v[168:171], v165 offset:52224
	s_add_u32 s30, s30, 0x40000
	s_addc_u32 s31, s31, 0
	s_mov_b32 m0, s47
	ds_read_b128 v[172:175], v188 offset:32768
	ds_read_b128 v[176:179], v188 offset:33792
	ds_read_b128 v[180:183], v188 offset:34816
	ds_read_b128 v[190:193], v188 offset:35840
	ds_read_b128 v[194:197], v188 offset:36864
	ds_read_b128 v[198:201], v188 offset:37888
	ds_read_b128 v[202:205], v188 offset:38912
	global_load_lds_dwordx4 v162, s[30:31]
	s_mov_b32 m0, s48
	ds_read_b128 v[206:209], v188 offset:39936
	global_load_lds_dwordx4 v160, s[30:31]
	s_waitcnt vmcnt(8) lgkmcnt(0)
	s_barrier
	v_mfma_f32_16x16x32_bf16 v[126:129], v[130:133], v[172:175], v[126:129]
	v_mfma_f32_16x16x32_bf16 v[122:125], v[138:141], v[172:175], v[122:125]
	v_mfma_f32_16x16x32_bf16 v[114:117], v[130:133], v[180:183], v[114:117]
	v_mfma_f32_16x16x32_bf16 v[106:109], v[138:141], v[180:183], v[106:109]
	v_mfma_f32_16x16x32_bf16 v[98:101], v[130:133], v[194:197], v[98:101]
	v_mfma_f32_16x16x32_bf16 v[90:93], v[138:141], v[194:197], v[90:93]
	v_mfma_f32_16x16x32_bf16 v[82:85], v[130:133], v[202:205], v[82:85]
	v_mfma_f32_16x16x32_bf16 v[74:77], v[138:141], v[202:205], v[74:77]
	v_mfma_f32_16x16x32_bf16 v[126:129], v[134:137], v[176:179], v[126:129]
	v_mfma_f32_16x16x32_bf16 v[122:125], v[142:145], v[176:179], v[122:125]
	v_mfma_f32_16x16x32_bf16 v[114:117], v[134:137], v[190:193], v[114:117]
	v_mfma_f32_16x16x32_bf16 v[106:109], v[142:145], v[190:193], v[106:109]
	v_mfma_f32_16x16x32_bf16 v[98:101], v[134:137], v[198:201], v[98:101]
	v_mfma_f32_16x16x32_bf16 v[90:93], v[142:145], v[198:201], v[90:93]
	v_mfma_f32_16x16x32_bf16 v[82:85], v[134:137], v[206:209], v[82:85]
	v_mfma_f32_16x16x32_bf16 v[74:77], v[142:145], v[206:209], v[74:77]
	v_mfma_f32_16x16x32_bf16 v[118:121], v[146:149], v[172:175], v[118:121]
	v_mfma_f32_16x16x32_bf16 v[110:113], v[154:157], v[172:175], v[110:113]
	v_mfma_f32_16x16x32_bf16 v[102:105], v[146:149], v[180:183], v[102:105]
	v_mfma_f32_16x16x32_bf16 v[94:97], v[154:157], v[180:183], v[94:97]
	v_mfma_f32_16x16x32_bf16 v[86:89], v[146:149], v[194:197], v[86:89]
	v_mfma_f32_16x16x32_bf16 v[78:81], v[154:157], v[194:197], v[78:81]
	v_mfma_f32_16x16x32_bf16 v[70:73], v[146:149], v[202:205], v[70:73]
	v_mfma_f32_16x16x32_bf16 v[66:69], v[154:157], v[202:205], v[66:69]
	v_mfma_f32_16x16x32_bf16 v[118:121], v[150:153], v[176:179], v[118:121]
	v_mfma_f32_16x16x32_bf16 v[110:113], v[168:171], v[176:179], v[110:113]
	v_mfma_f32_16x16x32_bf16 v[102:105], v[150:153], v[190:193], v[102:105]
	v_mfma_f32_16x16x32_bf16 v[94:97], v[168:171], v[190:193], v[94:97]
	v_mfma_f32_16x16x32_bf16 v[86:89], v[150:153], v[198:201], v[86:89]
	v_mfma_f32_16x16x32_bf16 v[78:81], v[168:171], v[198:201], v[78:81]
	v_mfma_f32_16x16x32_bf16 v[70:73], v[150:153], v[206:209], v[70:73]
	v_mfma_f32_16x16x32_bf16 v[66:69], v[168:171], v[206:209], v[66:69]
	s_barrier
	s_add_i32 s30, s43, s44
	v_lshl_add_u64 v[216:217], v[216:217], 0, s[56:57]
	s_mov_b32 m0, s30
	ds_read_b128 v[172:175], v188 offset:49152
	ds_read_b128 v[176:179], v188 offset:50176
	ds_read_b128 v[180:183], v188 offset:51200
	ds_read_b128 v[190:193], v188 offset:52224
	ds_read_b128 v[194:197], v188 offset:53248
	ds_read_b128 v[198:201], v188 offset:54272
	ds_read_b128 v[202:205], v188 offset:55296
	ds_read_b128 v[206:209], v188 offset:56320
	global_load_lds_dwordx4 v[216:217], off
	s_add_i32 m0, s30, 0x2000
	s_add_u32 s28, s28, 0x40080
	v_lshl_add_u64 v[216:217], v[218:219], 0, s[56:57]
	s_addc_u32 s29, s29, 0
	s_add_i32 s30, s58, s44
	global_load_lds_dwordx4 v[216:217], off
	s_mov_b32 m0, s30
	s_nop 0
	global_load_lds_dwordx4 v0, s[28:29]
	s_add_i32 m0, s30, 0x2000
	s_nop 0
	global_load_lds_dwordx4 v158, s[28:29]
	s_mov_b32 m0, s49
	v_lshl_add_u64 v[216:217], v[220:221], 0, s[56:57]
	global_load_lds_dwordx4 v[216:217], off
	s_mov_b32 m0, s52
	v_lshl_add_u64 v[216:217], v[222:223], 0, s[56:57]
	global_load_lds_dwordx4 v[216:217], off
	s_waitcnt vmcnt(8) lgkmcnt(0)
	s_barrier
	v_mfma_f32_16x16x32_bf16 v[62:65], v[130:133], v[172:175], v[62:65]
	v_mfma_f32_16x16x32_bf16 v[58:61], v[138:141], v[172:175], v[58:61]
	v_mfma_f32_16x16x32_bf16 v[50:53], v[130:133], v[180:183], v[50:53]
	v_mfma_f32_16x16x32_bf16 v[42:45], v[138:141], v[180:183], v[42:45]
	v_mfma_f32_16x16x32_bf16 v[34:37], v[130:133], v[194:197], v[34:37]
	v_mfma_f32_16x16x32_bf16 v[26:29], v[138:141], v[194:197], v[26:29]
	v_mfma_f32_16x16x32_bf16 v[18:21], v[130:133], v[202:205], v[18:21]
	v_mfma_f32_16x16x32_bf16 v[10:13], v[138:141], v[202:205], v[10:13]
	v_mfma_f32_16x16x32_bf16 v[62:65], v[134:137], v[176:179], v[62:65]
	v_mfma_f32_16x16x32_bf16 v[58:61], v[142:145], v[176:179], v[58:61]
	v_mfma_f32_16x16x32_bf16 v[50:53], v[134:137], v[190:193], v[50:53]
	v_mfma_f32_16x16x32_bf16 v[42:45], v[142:145], v[190:193], v[42:45]
	v_mfma_f32_16x16x32_bf16 v[34:37], v[134:137], v[198:201], v[34:37]
	v_mfma_f32_16x16x32_bf16 v[26:29], v[142:145], v[198:201], v[26:29]
	v_mfma_f32_16x16x32_bf16 v[18:21], v[134:137], v[206:209], v[18:21]
	v_mfma_f32_16x16x32_bf16 v[10:13], v[142:145], v[206:209], v[10:13]
	v_mfma_f32_16x16x32_bf16 v[54:57], v[146:149], v[172:175], v[54:57]
	v_mfma_f32_16x16x32_bf16 v[46:49], v[154:157], v[172:175], v[46:49]
	v_mfma_f32_16x16x32_bf16 v[38:41], v[146:149], v[180:183], v[38:41]
	v_mfma_f32_16x16x32_bf16 v[30:33], v[154:157], v[180:183], v[30:33]
	v_mfma_f32_16x16x32_bf16 v[22:25], v[146:149], v[194:197], v[22:25]
	v_mfma_f32_16x16x32_bf16 v[14:17], v[154:157], v[194:197], v[14:17]
	v_mfma_f32_16x16x32_bf16 v[6:9], v[146:149], v[202:205], v[6:9]
	v_mfma_f32_16x16x32_bf16 v[2:5], v[154:157], v[202:205], v[2:5]
	v_mfma_f32_16x16x32_bf16 v[54:57], v[150:153], v[176:179], v[54:57]
	v_mfma_f32_16x16x32_bf16 v[46:49], v[168:171], v[176:179], v[46:49]
	v_mfma_f32_16x16x32_bf16 v[38:41], v[150:153], v[190:193], v[38:41]
	v_mfma_f32_16x16x32_bf16 v[30:33], v[168:171], v[190:193], v[30:33]
	v_mfma_f32_16x16x32_bf16 v[22:25], v[150:153], v[198:201], v[22:25]
	v_mfma_f32_16x16x32_bf16 v[14:17], v[168:171], v[198:201], v[14:17]
	v_mfma_f32_16x16x32_bf16 v[6:9], v[150:153], v[206:209], v[6:9]
	v_mfma_f32_16x16x32_bf16 v[2:5], v[168:171], v[206:209], v[2:5]
	s_barrier
	s_add_i32 s42, s42, 2
	s_add_u32 s23, s23, 0x100
	s_addc_u32 s33, s33, 0
	s_add_u32 s6, s6, 0x100
	s_addc_u32 s7, s7, 0
	s_cmp_gt_u32 s42, 13
	s_cbranch_scc0 .LBB0_417


.LBB0_420:
	v_mov_b32_e32 v200, 0
	v_mov_b32_e32 v201, 0
	v_mov_b32_e32 v202, 0
	v_mov_b32_e32 v203, 0
	v_lshl_add_u32 v182, s4, 8, v185
	s_cmp_gt_u32 s62, 3
	s_cselect_b64 s[4:5], -1, 0
	v_cndmask_b32_e64 v190, v230, 1.0, s[4:5]
	s_waitcnt vmcnt(8)
	v_add_f32_e32 v240, v240, v241
	v_add_f32_e32 v242, v242, v243
	v_add_f32_e32 v240, v240, v242
	v_fmamk_f32 v240, v240, 0x3a800000, v226
	v_rsq_f32_e32 v240, v240
	v_add_f32_e32 v244, v244, v245
	v_add_f32_e32 v184, v184, v189
	v_add_f32_e32 v244, v244, v184
	v_fmamk_f32 v244, v244, 0x3a800000, v226
	v_rsq_f32_e32 v244, v244
	v_and_b32_e32 v191, 15, v185
	v_lshlrev_b32_e32 v191, 2, v191
	v_add_u32_e32 v192, 64, v191
	v_add_u32_e32 v193, 0x80, v191
	v_add_u32_e32 v194, 0xc0, v191
	v_mul_f32_e32 v240, v240, v190
	v_mul_f32_e32 v244, v244, v190
	ds_bpermute_b32 v144, v191, v240
	ds_bpermute_b32 v146, v191, v244
	ds_bpermute_b32 v148, v192, v240
	ds_bpermute_b32 v150, v192, v244
	ds_bpermute_b32 v152, v193, v240
	ds_bpermute_b32 v154, v193, v244
	ds_bpermute_b32 v156, v194, v240
	ds_bpermute_b32 v168, v194, v244
	v_lshl_or_b32 v170, s62, 8, v187
	v_lshlrev_b32_e32 v170, 1, v170
	v_mov_b32_e32 v171, 0
	v_mov_b64_e32 v[172:173], s[14:15]
	v_mad_i64_i32 v[172:173], s[4:5], v182, s69, v[172:173]
	v_lshl_add_u64 v[172:173], v[172:173], 0, v[170:171]
	s_waitcnt lgkmcnt(0)
	v_pk_mul_f32 v[126:127], v[126:127], v[144:145] op_sel_hi:[1,0]
	v_pk_mul_f32 v[128:129], v[128:129], v[144:145] op_sel_hi:[1,0]
	v_pk_mul_f32 v[122:123], v[122:123], v[144:145] op_sel_hi:[1,0]
	v_pk_mul_f32 v[124:125], v[124:125], v[144:145] op_sel_hi:[1,0]
	v_cvt_pk_bf16_f32 v126, v126, v127
	v_cvt_pk_bf16_f32 v127, v128, v129
	v_cvt_pk_bf16_f32 v128, v122, v123
	v_cvt_pk_bf16_f32 v129, v124, v125
	global_store_dwordx4 v[172:173], v[126:129], off
	v_pk_mul_f32 v[118:119], v[118:119], v[144:145] op_sel_hi:[1,0]
	v_pk_mul_f32 v[120:121], v[120:121], v[144:145] op_sel_hi:[1,0]
	v_pk_mul_f32 v[110:111], v[110:111], v[144:145] op_sel_hi:[1,0]
	v_pk_mul_f32 v[112:113], v[112:113], v[144:145] op_sel_hi:[1,0]
	v_cvt_pk_bf16_f32 v118, v118, v119
	v_cvt_pk_bf16_f32 v119, v120, v121
	v_cvt_pk_bf16_f32 v120, v110, v111
	v_cvt_pk_bf16_f32 v121, v112, v113
	global_store_dwordx4 v[172:173], v[118:121], off offset:256
	s_mov_b64 s[42:43], 0xa000
	v_lshl_add_u64 v[176:177], v[172:173], 0, s[42:43]
	v_pk_mul_f32 v[114:115], v[114:115], v[146:147] op_sel_hi:[1,0]
	v_pk_mul_f32 v[116:117], v[116:117], v[146:147] op_sel_hi:[1,0]
	v_pk_mul_f32 v[106:107], v[106:107], v[146:147] op_sel_hi:[1,0]
	v_pk_mul_f32 v[108:109], v[108:109], v[146:147] op_sel_hi:[1,0]
	v_cvt_pk_bf16_f32 v114, v114, v115
	v_cvt_pk_bf16_f32 v115, v116, v117
	v_cvt_pk_bf16_f32 v116, v106, v107
	v_cvt_pk_bf16_f32 v117, v108, v109
	global_store_dwordx4 v[176:177], v[114:117], off
	v_pk_mul_f32 v[102:103], v[102:103], v[146:147] op_sel_hi:[1,0]
	v_pk_mul_f32 v[104:105], v[104:105], v[146:147] op_sel_hi:[1,0]
	v_pk_mul_f32 v[94:95], v[94:95], v[146:147] op_sel_hi:[1,0]
	v_pk_mul_f32 v[96:97], v[96:97], v[146:147] op_sel_hi:[1,0]
	v_cvt_pk_bf16_f32 v102, v102, v103
	v_cvt_pk_bf16_f32 v103, v104, v105
	v_cvt_pk_bf16_f32 v104, v94, v95
	v_cvt_pk_bf16_f32 v105, v96, v97
	global_store_dwordx4 v[176:177], v[102:105], off offset:256
	s_and_b64 vcc, exec, s[18:19]
	s_cbranch_vccz .Lalign_e1o
	s_barrier
.Lalign_e1o:
	s_mov_b64 s[42:43], 0x14000
	v_lshl_add_u64 v[174:175], v[172:173], 0, s[42:43]
	v_pk_mul_f32 v[98:99], v[98:99], v[148:149] op_sel_hi:[1,0]
	v_pk_mul_f32 v[100:101], v[100:101], v[148:149] op_sel_hi:[1,0]
	v_pk_mul_f32 v[90:91], v[90:91], v[148:149] op_sel_hi:[1,0]
	v_pk_mul_f32 v[92:93], v[92:93], v[148:149] op_sel_hi:[1,0]
	v_cvt_pk_bf16_f32 v98, v98, v99
	v_cvt_pk_bf16_f32 v99, v100, v101
	v_cvt_pk_bf16_f32 v100, v90, v91
	v_cvt_pk_bf16_f32 v101, v92, v93
	global_store_dwordx4 v[174:175], v[98:101], off
	v_pk_mul_f32 v[86:87], v[86:87], v[148:149] op_sel_hi:[1,0]
	v_pk_mul_f32 v[88:89], v[88:89], v[148:149] op_sel_hi:[1,0]
	v_pk_mul_f32 v[78:79], v[78:79], v[148:149] op_sel_hi:[1,0]
	v_pk_mul_f32 v[80:81], v[80:81], v[148:149] op_sel_hi:[1,0]
	v_cvt_pk_bf16_f32 v86, v86, v87
	v_cvt_pk_bf16_f32 v87, v88, v89
	v_cvt_pk_bf16_f32 v88, v78, v79
	v_cvt_pk_bf16_f32 v89, v80, v81
	global_store_dwordx4 v[174:175], v[86:89], off offset:256
	s_mov_b64 s[42:43], 0x1e000
	v_lshl_add_u64 v[176:177], v[172:173], 0, s[42:43]
	v_pk_mul_f32 v[82:83], v[82:83], v[150:151] op_sel_hi:[1,0]
	v_pk_mul_f32 v[84:85], v[84:85], v[150:151] op_sel_hi:[1,0]
	v_pk_mul_f32 v[74:75], v[74:75], v[150:151] op_sel_hi:[1,0]
	v_pk_mul_f32 v[76:77], v[76:77], v[150:151] op_sel_hi:[1,0]
	v_cvt_pk_bf16_f32 v82, v82, v83
	v_cvt_pk_bf16_f32 v83, v84, v85
	v_cvt_pk_bf16_f32 v84, v74, v75
	v_cvt_pk_bf16_f32 v85, v76, v77
	global_store_dwordx4 v[176:177], v[82:85], off
	v_pk_mul_f32 v[70:71], v[70:71], v[150:151] op_sel_hi:[1,0]
	v_pk_mul_f32 v[72:73], v[72:73], v[150:151] op_sel_hi:[1,0]
	v_pk_mul_f32 v[66:67], v[66:67], v[150:151] op_sel_hi:[1,0]
	v_pk_mul_f32 v[68:69], v[68:69], v[150:151] op_sel_hi:[1,0]
	v_cvt_pk_bf16_f32 v70, v70, v71
	v_cvt_pk_bf16_f32 v71, v72, v73
	v_cvt_pk_bf16_f32 v72, v66, v67
	v_cvt_pk_bf16_f32 v73, v68, v69
	global_store_dwordx4 v[176:177], v[70:73], off offset:256
	s_mov_b64 s[42:43], 0x50000
	v_lshl_add_u64 v[174:175], v[172:173], 0, s[42:43]
	v_pk_mul_f32 v[62:63], v[62:63], v[152:153] op_sel_hi:[1,0]
	v_pk_mul_f32 v[64:65], v[64:65], v[152:153] op_sel_hi:[1,0]
	v_pk_mul_f32 v[58:59], v[58:59], v[152:153] op_sel_hi:[1,0]
	v_pk_mul_f32 v[60:61], v[60:61], v[152:153] op_sel_hi:[1,0]
	v_cvt_pk_bf16_f32 v62, v62, v63
	v_cvt_pk_bf16_f32 v63, v64, v65
	v_cvt_pk_bf16_f32 v64, v58, v59
	v_cvt_pk_bf16_f32 v65, v60, v61
	global_store_dwordx4 v[174:175], v[62:65], off
	v_pk_mul_f32 v[54:55], v[54:55], v[152:153] op_sel_hi:[1,0]
	v_pk_mul_f32 v[56:57], v[56:57], v[152:153] op_sel_hi:[1,0]
	v_pk_mul_f32 v[46:47], v[46:47], v[152:153] op_sel_hi:[1,0]
	v_pk_mul_f32 v[48:49], v[48:49], v[152:153] op_sel_hi:[1,0]
	v_cvt_pk_bf16_f32 v54, v54, v55
	v_cvt_pk_bf16_f32 v55, v56, v57
	v_cvt_pk_bf16_f32 v56, v46, v47
	v_cvt_pk_bf16_f32 v57, v48, v49
	global_store_dwordx4 v[174:175], v[54:57], off offset:256
	s_mov_b64 s[42:43], 0x5a000
	v_lshl_add_u64 v[176:177], v[172:173], 0, s[42:43]
	v_pk_mul_f32 v[50:51], v[50:51], v[154:155] op_sel_hi:[1,0]
	v_pk_mul_f32 v[52:53], v[52:53], v[154:155] op_sel_hi:[1,0]
	v_pk_mul_f32 v[42:43], v[42:43], v[154:155] op_sel_hi:[1,0]
	v_pk_mul_f32 v[44:45], v[44:45], v[154:155] op_sel_hi:[1,0]
	v_cvt_pk_bf16_f32 v50, v50, v51
	v_cvt_pk_bf16_f32 v51, v52, v53
	v_cvt_pk_bf16_f32 v52, v42, v43
	v_cvt_pk_bf16_f32 v53, v44, v45
	global_store_dwordx4 v[176:177], v[50:53], off
	v_pk_mul_f32 v[38:39], v[38:39], v[154:155] op_sel_hi:[1,0]
	v_pk_mul_f32 v[40:41], v[40:41], v[154:155] op_sel_hi:[1,0]
	v_pk_mul_f32 v[30:31], v[30:31], v[154:155] op_sel_hi:[1,0]
	v_pk_mul_f32 v[32:33], v[32:33], v[154:155] op_sel_hi:[1,0]
	v_cvt_pk_bf16_f32 v38, v38, v39
	v_cvt_pk_bf16_f32 v39, v40, v41
	v_cvt_pk_bf16_f32 v40, v30, v31
	v_cvt_pk_bf16_f32 v41, v32, v33
	global_store_dwordx4 v[176:177], v[38:41], off offset:256
	s_mov_b64 s[42:43], 0x64000
	v_lshl_add_u64 v[174:175], v[172:173], 0, s[42:43]
	v_pk_mul_f32 v[34:35], v[34:35], v[156:157] op_sel_hi:[1,0]
	v_pk_mul_f32 v[36:37], v[36:37], v[156:157] op_sel_hi:[1,0]
	v_pk_mul_f32 v[26:27], v[26:27], v[156:157] op_sel_hi:[1,0]
	v_pk_mul_f32 v[28:29], v[28:29], v[156:157] op_sel_hi:[1,0]
	v_cvt_pk_bf16_f32 v34, v34, v35
	v_cvt_pk_bf16_f32 v35, v36, v37
	v_cvt_pk_bf16_f32 v36, v26, v27
	v_cvt_pk_bf16_f32 v37, v28, v29
	global_store_dwordx4 v[174:175], v[34:37], off
	v_pk_mul_f32 v[22:23], v[22:23], v[156:157] op_sel_hi:[1,0]
	v_pk_mul_f32 v[24:25], v[24:25], v[156:157] op_sel_hi:[1,0]
	v_pk_mul_f32 v[14:15], v[14:15], v[156:157] op_sel_hi:[1,0]
	v_pk_mul_f32 v[16:17], v[16:17], v[156:157] op_sel_hi:[1,0]
	v_cvt_pk_bf16_f32 v22, v22, v23
	v_cvt_pk_bf16_f32 v23, v24, v25
	v_cvt_pk_bf16_f32 v24, v14, v15
	v_cvt_pk_bf16_f32 v25, v16, v17
	global_store_dwordx4 v[174:175], v[22:25], off offset:256
	s_mov_b64 s[42:43], 0x6e000
	v_lshl_add_u64 v[176:177], v[172:173], 0, s[42:43]
	v_pk_mul_f32 v[18:19], v[18:19], v[168:169] op_sel_hi:[1,0]
	v_pk_mul_f32 v[20:21], v[20:21], v[168:169] op_sel_hi:[1,0]
	v_pk_mul_f32 v[10:11], v[10:11], v[168:169] op_sel_hi:[1,0]
	v_pk_mul_f32 v[12:13], v[12:13], v[168:169] op_sel_hi:[1,0]
	v_cvt_pk_bf16_f32 v18, v18, v19
	v_cvt_pk_bf16_f32 v19, v20, v21
	v_cvt_pk_bf16_f32 v20, v10, v11
	v_cvt_pk_bf16_f32 v21, v12, v13
	global_store_dwordx4 v[176:177], v[18:21], off
	v_pk_mul_f32 v[6:7], v[6:7], v[168:169] op_sel_hi:[1,0]
	v_pk_mul_f32 v[8:9], v[8:9], v[168:169] op_sel_hi:[1,0]
	v_pk_mul_f32 v[2:3], v[2:3], v[168:169] op_sel_hi:[1,0]
	v_pk_mul_f32 v[4:5], v[4:5], v[168:169] op_sel_hi:[1,0]
	v_cvt_pk_bf16_f32 v6, v6, v7
	v_cvt_pk_bf16_f32 v7, v8, v9
	v_cvt_pk_bf16_f32 v8, v2, v3
	v_cvt_pk_bf16_f32 v9, v4, v5
	global_store_dwordx4 v[176:177], v[6:9], off offset:256
	s_nop 3
	v_mfma_f32_32x32x16_bf16 v[2:17], v[200:203], v[200:203], 0
	v_mfma_f32_32x32x16_bf16 v[18:33], v[200:203], v[200:203], 0
	v_mfma_f32_32x32x16_bf16 v[34:49], v[200:203], v[200:203], 0
	v_mfma_f32_32x32x16_bf16 v[50:65], v[200:203], v[200:203], 0
	v_mfma_f32_32x32x16_bf16 v[66:81], v[200:203], v[200:203], 0
	v_mfma_f32_32x32x16_bf16 v[82:97], v[200:203], v[200:203], 0
	v_mfma_f32_32x32x16_bf16 v[98:113], v[200:203], v[200:203], 0
	v_mfma_f32_32x32x16_bf16 v[114:129], v[200:203], v[200:203], 0
	s_andn2_b64 vcc, exec, s[40:41]
	s_mov_b64 s[6:7], -1
	s_cbranch_vccnz .LBB0_413
	s_andn2_b64 vcc, exec, s[12:13]
	s_cbranch_vccnz .LBB0_412
	s_branch .LBB0_412

.LBB0_836:
	s_add_u32 s28, s6, 0xfffc0080
	s_addc_u32 s29, s7, -1
	s_add_i32 s41, 0, 0x10000
	s_cmp_eq_u32 s40, 12
	s_cselect_b32 s31, s5, s29
	s_cselect_b32 s30, s8, s28
	s_cselect_b32 s29, s9, s33
	s_cselect_b32 s28, s21, s23
	s_add_i32 s53, 0, 0x14000
	ds_read_b128 v[130:133], v165
	ds_read_b128 v[134:137], v165 offset:1024
	ds_read_b128 v[138:141], v165 offset:2048
	ds_read_b128 v[142:145], v165 offset:3072
	ds_read_b128 v[146:149], v165 offset:16384
	ds_read_b128 v[150:153], v165 offset:17408
	ds_read_b128 v[154:157], v165 offset:18432
	ds_read_b128 v[168:171], v165 offset:19456
	s_add_i32 m0, s43, 0xc000
	ds_read_b128 v[172:175], v188
	ds_read_b128 v[176:179], v188 offset:1024
	ds_read_b128 v[180:183], v188 offset:2048
	ds_read_b128 v[190:193], v188 offset:3072
	ds_read_b128 v[194:197], v188 offset:4096
	ds_read_b128 v[198:201], v188 offset:5120
	ds_read_b128 v[202:205], v188 offset:6144
	global_load_lds_dwordx4 v166, s[6:7]
	s_add_i32 m0, s43, 0xe000
	ds_read_b128 v[206:209], v188 offset:7168
	global_load_lds_dwordx4 v164, s[6:7]
	s_waitcnt vmcnt(8) lgkmcnt(0)
	s_barrier
	v_mfma_f32_16x16x32_bf16 v[126:129], v[130:133], v[172:175], v[126:129]
	v_mfma_f32_16x16x32_bf16 v[122:125], v[138:141], v[172:175], v[122:125]
	v_mfma_f32_16x16x32_bf16 v[114:117], v[130:133], v[180:183], v[114:117]
	v_mfma_f32_16x16x32_bf16 v[106:109], v[138:141], v[180:183], v[106:109]
	v_mfma_f32_16x16x32_bf16 v[98:101], v[130:133], v[194:197], v[98:101]
	v_mfma_f32_16x16x32_bf16 v[90:93], v[138:141], v[194:197], v[90:93]
	v_mfma_f32_16x16x32_bf16 v[82:85], v[130:133], v[202:205], v[82:85]
	v_mfma_f32_16x16x32_bf16 v[74:77], v[138:141], v[202:205], v[74:77]
	v_mfma_f32_16x16x32_bf16 v[126:129], v[134:137], v[176:179], v[126:129]
	v_mfma_f32_16x16x32_bf16 v[122:125], v[142:145], v[176:179], v[122:125]
	v_mfma_f32_16x16x32_bf16 v[114:117], v[134:137], v[190:193], v[114:117]
	v_mfma_f32_16x16x32_bf16 v[106:109], v[142:145], v[190:193], v[106:109]
	v_mfma_f32_16x16x32_bf16 v[98:101], v[134:137], v[198:201], v[98:101]
	v_mfma_f32_16x16x32_bf16 v[90:93], v[142:145], v[198:201], v[90:93]
	v_mfma_f32_16x16x32_bf16 v[82:85], v[134:137], v[206:209], v[82:85]
	v_mfma_f32_16x16x32_bf16 v[74:77], v[142:145], v[206:209], v[74:77]
	v_mfma_f32_16x16x32_bf16 v[118:121], v[146:149], v[172:175], v[118:121]
	v_mfma_f32_16x16x32_bf16 v[110:113], v[154:157], v[172:175], v[110:113]
	v_mfma_f32_16x16x32_bf16 v[102:105], v[146:149], v[180:183], v[102:105]
	v_mfma_f32_16x16x32_bf16 v[94:97], v[154:157], v[180:183], v[94:97]
	v_mfma_f32_16x16x32_bf16 v[86:89], v[146:149], v[194:197], v[86:89]
	v_mfma_f32_16x16x32_bf16 v[78:81], v[154:157], v[194:197], v[78:81]
	v_mfma_f32_16x16x32_bf16 v[70:73], v[146:149], v[202:205], v[70:73]
	v_mfma_f32_16x16x32_bf16 v[66:69], v[154:157], v[202:205], v[66:69]
	v_mfma_f32_16x16x32_bf16 v[118:121], v[150:153], v[176:179], v[118:121]
	v_mfma_f32_16x16x32_bf16 v[110:113], v[168:171], v[176:179], v[110:113]
	v_mfma_f32_16x16x32_bf16 v[102:105], v[150:153], v[190:193], v[102:105]
	v_mfma_f32_16x16x32_bf16 v[94:97], v[168:171], v[190:193], v[94:97]
	v_mfma_f32_16x16x32_bf16 v[86:89], v[150:153], v[198:201], v[86:89]
	v_mfma_f32_16x16x32_bf16 v[78:81], v[168:171], v[198:201], v[78:81]
	v_mfma_f32_16x16x32_bf16 v[70:73], v[150:153], v[206:209], v[70:73]
	v_mfma_f32_16x16x32_bf16 v[66:69], v[168:171], v[206:209], v[66:69]
	s_barrier
	s_add_i32 s41, s41, s42
	v_lshl_add_u64 v[216:217], s[28:29], 0, v[0:1]
	s_mov_b32 m0, s41
	ds_read_b128 v[172:175], v188 offset:16384
	ds_read_b128 v[176:179], v188 offset:17408
	ds_read_b128 v[180:183], v188 offset:18432
	ds_read_b128 v[190:193], v188 offset:19456
	ds_read_b128 v[194:197], v188 offset:20480
	ds_read_b128 v[198:201], v188 offset:21504
	ds_read_b128 v[202:205], v188 offset:22528
	ds_read_b128 v[206:209], v188 offset:23552
	global_load_lds_dwordx4 v0, s[28:29]
	s_add_i32 m0, s41, 0x2000
	s_add_u32 s58, s28, 0x40000
	v_lshl_add_u64 v[218:219], s[28:29], 0, v[158:159]
	s_addc_u32 s59, s29, 0
	s_add_i32 s41, s53, s42
	global_load_lds_dwordx4 v158, s[28:29]
	s_mov_b32 m0, s41
	v_lshl_add_u64 v[222:223], s[30:31], 0, v[160:161]
	global_load_lds_dwordx4 v0, s[58:59]
	s_add_i32 m0, s41, 0x2000
	s_nop 0
	global_load_lds_dwordx4 v158, s[58:59]
	s_mov_b32 m0, s43
	v_lshl_add_u64 v[220:221], s[30:31], 0, v[162:163]
	global_load_lds_dwordx4 v162, s[30:31]
	s_mov_b32 m0, s44
	s_nop 0
	global_load_lds_dwordx4 v160, s[30:31]
	s_waitcnt vmcnt(8) lgkmcnt(0)
	s_barrier
	v_mfma_f32_16x16x32_bf16 v[62:65], v[130:133], v[172:175], v[62:65]
	v_mfma_f32_16x16x32_bf16 v[58:61], v[138:141], v[172:175], v[58:61]
	v_mfma_f32_16x16x32_bf16 v[50:53], v[130:133], v[180:183], v[50:53]
	v_mfma_f32_16x16x32_bf16 v[42:45], v[138:141], v[180:183], v[42:45]
	v_mfma_f32_16x16x32_bf16 v[34:37], v[130:133], v[194:197], v[34:37]
	v_mfma_f32_16x16x32_bf16 v[26:29], v[138:141], v[194:197], v[26:29]
	v_mfma_f32_16x16x32_bf16 v[18:21], v[130:133], v[202:205], v[18:21]
	v_mfma_f32_16x16x32_bf16 v[10:13], v[138:141], v[202:205], v[10:13]
	v_mfma_f32_16x16x32_bf16 v[62:65], v[134:137], v[176:179], v[62:65]
	v_mfma_f32_16x16x32_bf16 v[58:61], v[142:145], v[176:179], v[58:61]
	v_mfma_f32_16x16x32_bf16 v[50:53], v[134:137], v[190:193], v[50:53]
	v_mfma_f32_16x16x32_bf16 v[42:45], v[142:145], v[190:193], v[42:45]
	v_mfma_f32_16x16x32_bf16 v[34:37], v[134:137], v[198:201], v[34:37]
	v_mfma_f32_16x16x32_bf16 v[26:29], v[142:145], v[198:201], v[26:29]
	v_mfma_f32_16x16x32_bf16 v[18:21], v[134:137], v[206:209], v[18:21]
	v_mfma_f32_16x16x32_bf16 v[10:13], v[142:145], v[206:209], v[10:13]
	v_mfma_f32_16x16x32_bf16 v[54:57], v[146:149], v[172:175], v[54:57]
	v_mfma_f32_16x16x32_bf16 v[46:49], v[154:157], v[172:175], v[46:49]
	v_mfma_f32_16x16x32_bf16 v[38:41], v[146:149], v[180:183], v[38:41]
	v_mfma_f32_16x16x32_bf16 v[30:33], v[154:157], v[180:183], v[30:33]
	v_mfma_f32_16x16x32_bf16 v[22:25], v[146:149], v[194:197], v[22:25]
	v_mfma_f32_16x16x32_bf16 v[14:17], v[154:157], v[194:197], v[14:17]
	v_mfma_f32_16x16x32_bf16 v[6:9], v[146:149], v[202:205], v[6:9]
	v_mfma_f32_16x16x32_bf16 v[2:5], v[154:157], v[202:205], v[2:5]
	v_mfma_f32_16x16x32_bf16 v[54:57], v[150:153], v[176:179], v[54:57]
	v_mfma_f32_16x16x32_bf16 v[46:49], v[168:171], v[176:179], v[46:49]
	v_mfma_f32_16x16x32_bf16 v[38:41], v[150:153], v[190:193], v[38:41]
	v_mfma_f32_16x16x32_bf16 v[30:33], v[168:171], v[190:193], v[30:33]
	v_mfma_f32_16x16x32_bf16 v[22:25], v[150:153], v[198:201], v[22:25]
	v_mfma_f32_16x16x32_bf16 v[14:17], v[168:171], v[198:201], v[14:17]
	v_mfma_f32_16x16x32_bf16 v[6:9], v[150:153], v[206:209], v[6:9]
	v_mfma_f32_16x16x32_bf16 v[2:5], v[168:171], v[206:209], v[2:5]
	s_barrier
	s_add_i32 s41, 0, 0x18000
	s_add_i32 s53, 0, 0x1c000
	ds_read_b128 v[130:133], v165 offset:32768
	ds_read_b128 v[134:137], v165 offset:33792
	ds_read_b128 v[138:141], v165 offset:34816
	ds_read_b128 v[142:145], v165 offset:35840
	ds_read_b128 v[146:149], v165 offset:49152
	ds_read_b128 v[150:153], v165 offset:50176
	ds_read_b128 v[154:157], v165 offset:51200
	ds_read_b128 v[168:171], v165 offset:52224
	s_add_u32 s30, s30, 0x40000
	s_addc_u32 s31, s31, 0
	s_mov_b32 m0, s45
	ds_read_b128 v[172:175], v188 offset:32768
	ds_read_b128 v[176:179], v188 offset:33792
	ds_read_b128 v[180:183], v188 offset:34816
	ds_read_b128 v[190:193], v188 offset:35840
	ds_read_b128 v[194:197], v188 offset:36864
	ds_read_b128 v[198:201], v188 offset:37888
	ds_read_b128 v[202:205], v188 offset:38912
	global_load_lds_dwordx4 v162, s[30:31]
	s_mov_b32 m0, s46
	ds_read_b128 v[206:209], v188 offset:39936
	global_load_lds_dwordx4 v160, s[30:31]
	s_waitcnt vmcnt(8) lgkmcnt(0)
	s_barrier
	v_mfma_f32_16x16x32_bf16 v[126:129], v[130:133], v[172:175], v[126:129]
	v_mfma_f32_16x16x32_bf16 v[122:125], v[138:141], v[172:175], v[122:125]
	v_mfma_f32_16x16x32_bf16 v[114:117], v[130:133], v[180:183], v[114:117]
	v_mfma_f32_16x16x32_bf16 v[106:109], v[138:141], v[180:183], v[106:109]
	v_mfma_f32_16x16x32_bf16 v[98:101], v[130:133], v[194:197], v[98:101]
	v_mfma_f32_16x16x32_bf16 v[90:93], v[138:141], v[194:197], v[90:93]
	v_mfma_f32_16x16x32_bf16 v[82:85], v[130:133], v[202:205], v[82:85]
	v_mfma_f32_16x16x32_bf16 v[74:77], v[138:141], v[202:205], v[74:77]
	v_mfma_f32_16x16x32_bf16 v[126:129], v[134:137], v[176:179], v[126:129]
	v_mfma_f32_16x16x32_bf16 v[122:125], v[142:145], v[176:179], v[122:125]
	v_mfma_f32_16x16x32_bf16 v[114:117], v[134:137], v[190:193], v[114:117]
	v_mfma_f32_16x16x32_bf16 v[106:109], v[142:145], v[190:193], v[106:109]
	v_mfma_f32_16x16x32_bf16 v[98:101], v[134:137], v[198:201], v[98:101]
	v_mfma_f32_16x16x32_bf16 v[90:93], v[142:145], v[198:201], v[90:93]
	v_mfma_f32_16x16x32_bf16 v[82:85], v[134:137], v[206:209], v[82:85]
	v_mfma_f32_16x16x32_bf16 v[74:77], v[142:145], v[206:209], v[74:77]
	v_mfma_f32_16x16x32_bf16 v[118:121], v[146:149], v[172:175], v[118:121]
	v_mfma_f32_16x16x32_bf16 v[110:113], v[154:157], v[172:175], v[110:113]
	v_mfma_f32_16x16x32_bf16 v[102:105], v[146:149], v[180:183], v[102:105]
	v_mfma_f32_16x16x32_bf16 v[94:97], v[154:157], v[180:183], v[94:97]
	v_mfma_f32_16x16x32_bf16 v[86:89], v[146:149], v[194:197], v[86:89]
	v_mfma_f32_16x16x32_bf16 v[78:81], v[154:157], v[194:197], v[78:81]
	v_mfma_f32_16x16x32_bf16 v[70:73], v[146:149], v[202:205], v[70:73]
	v_mfma_f32_16x16x32_bf16 v[66:69], v[154:157], v[202:205], v[66:69]
	v_mfma_f32_16x16x32_bf16 v[118:121], v[150:153], v[176:179], v[118:121]
	v_mfma_f32_16x16x32_bf16 v[110:113], v[168:171], v[176:179], v[110:113]
	v_mfma_f32_16x16x32_bf16 v[102:105], v[150:153], v[190:193], v[102:105]
	v_mfma_f32_16x16x32_bf16 v[94:97], v[168:171], v[190:193], v[94:97]
	v_mfma_f32_16x16x32_bf16 v[86:89], v[150:153], v[198:201], v[86:89]
	v_mfma_f32_16x16x32_bf16 v[78:81], v[168:171], v[198:201], v[78:81]
	v_mfma_f32_16x16x32_bf16 v[70:73], v[150:153], v[206:209], v[70:73]
	v_mfma_f32_16x16x32_bf16 v[66:69], v[168:171], v[206:209], v[66:69]
	s_barrier
	s_add_i32 s30, s41, s42
	v_lshl_add_u64 v[216:217], v[216:217], 0, s[56:57]
	s_mov_b32 m0, s30
	ds_read_b128 v[172:175], v188 offset:49152
	ds_read_b128 v[176:179], v188 offset:50176
	ds_read_b128 v[180:183], v188 offset:51200
	ds_read_b128 v[190:193], v188 offset:52224
	ds_read_b128 v[194:197], v188 offset:53248
	ds_read_b128 v[198:201], v188 offset:54272
	ds_read_b128 v[202:205], v188 offset:55296
	ds_read_b128 v[206:209], v188 offset:56320
	global_load_lds_dwordx4 v[216:217], off
	s_add_i32 m0, s30, 0x2000
	s_add_u32 s28, s28, 0x40080
	v_lshl_add_u64 v[216:217], v[218:219], 0, s[56:57]
	s_addc_u32 s29, s29, 0
	s_add_i32 s30, s53, s42
	global_load_lds_dwordx4 v[216:217], off
	s_mov_b32 m0, s30
	s_nop 0
	global_load_lds_dwordx4 v0, s[28:29]
	s_add_i32 m0, s30, 0x2000
	s_nop 0
	global_load_lds_dwordx4 v158, s[28:29]
	s_mov_b32 m0, s47
	v_lshl_add_u64 v[216:217], v[220:221], 0, s[56:57]
	global_load_lds_dwordx4 v[216:217], off
	s_mov_b32 m0, s48
	v_lshl_add_u64 v[216:217], v[222:223], 0, s[56:57]
	global_load_lds_dwordx4 v[216:217], off
	s_waitcnt vmcnt(8) lgkmcnt(0)
	s_barrier
	v_mfma_f32_16x16x32_bf16 v[62:65], v[130:133], v[172:175], v[62:65]
	v_mfma_f32_16x16x32_bf16 v[58:61], v[138:141], v[172:175], v[58:61]
	v_mfma_f32_16x16x32_bf16 v[50:53], v[130:133], v[180:183], v[50:53]
	v_mfma_f32_16x16x32_bf16 v[42:45], v[138:141], v[180:183], v[42:45]
	v_mfma_f32_16x16x32_bf16 v[34:37], v[130:133], v[194:197], v[34:37]
	v_mfma_f32_16x16x32_bf16 v[26:29], v[138:141], v[194:197], v[26:29]
	v_mfma_f32_16x16x32_bf16 v[18:21], v[130:133], v[202:205], v[18:21]
	v_mfma_f32_16x16x32_bf16 v[10:13], v[138:141], v[202:205], v[10:13]
	v_mfma_f32_16x16x32_bf16 v[62:65], v[134:137], v[176:179], v[62:65]
	v_mfma_f32_16x16x32_bf16 v[58:61], v[142:145], v[176:179], v[58:61]
	v_mfma_f32_16x16x32_bf16 v[50:53], v[134:137], v[190:193], v[50:53]
	v_mfma_f32_16x16x32_bf16 v[42:45], v[142:145], v[190:193], v[42:45]
	v_mfma_f32_16x16x32_bf16 v[34:37], v[134:137], v[198:201], v[34:37]
	v_mfma_f32_16x16x32_bf16 v[26:29], v[142:145], v[198:201], v[26:29]
	v_mfma_f32_16x16x32_bf16 v[18:21], v[134:137], v[206:209], v[18:21]
	v_mfma_f32_16x16x32_bf16 v[10:13], v[142:145], v[206:209], v[10:13]
	v_mfma_f32_16x16x32_bf16 v[54:57], v[146:149], v[172:175], v[54:57]
	v_mfma_f32_16x16x32_bf16 v[46:49], v[154:157], v[172:175], v[46:49]
	v_mfma_f32_16x16x32_bf16 v[38:41], v[146:149], v[180:183], v[38:41]
	v_mfma_f32_16x16x32_bf16 v[30:33], v[154:157], v[180:183], v[30:33]
	v_mfma_f32_16x16x32_bf16 v[22:25], v[146:149], v[194:197], v[22:25]
	v_mfma_f32_16x16x32_bf16 v[14:17], v[154:157], v[194:197], v[14:17]
	v_mfma_f32_16x16x32_bf16 v[6:9], v[146:149], v[202:205], v[6:9]
	v_mfma_f32_16x16x32_bf16 v[2:5], v[154:157], v[202:205], v[2:5]
	v_mfma_f32_16x16x32_bf16 v[54:57], v[150:153], v[176:179], v[54:57]
	v_mfma_f32_16x16x32_bf16 v[46:49], v[168:171], v[176:179], v[46:49]
	v_mfma_f32_16x16x32_bf16 v[38:41], v[150:153], v[190:193], v[38:41]
	v_mfma_f32_16x16x32_bf16 v[30:33], v[168:171], v[190:193], v[30:33]
	v_mfma_f32_16x16x32_bf16 v[22:25], v[150:153], v[198:201], v[22:25]
	v_mfma_f32_16x16x32_bf16 v[14:17], v[168:171], v[198:201], v[14:17]
	v_mfma_f32_16x16x32_bf16 v[6:9], v[150:153], v[206:209], v[6:9]
	v_mfma_f32_16x16x32_bf16 v[2:5], v[168:171], v[206:209], v[2:5]
	s_barrier
	s_add_i32 s40, s40, 2
	s_add_u32 s23, s23, 0x100
	s_addc_u32 s33, s33, 0
	s_add_u32 s6, s6, 0x100
	s_addc_u32 s7, s7, 0
	s_cmp_gt_u32 s40, 13
	s_cbranch_scc0 .LBB0_836


.LBB0_839:
	v_mov_b32_e32 v200, 0
	v_mov_b32_e32 v201, 0
	v_mov_b32_e32 v202, 0
	v_mov_b32_e32 v203, 0
	v_lshl_add_u32 v182, s4, 8, v185
	s_lshl_b32 s4, 1, s52
	s_and_b32 s4, s4, 0x18f
	s_cmp_eq_u32 s4, 0
	s_cselect_b64 s[4:5], -1, 0
	v_cndmask_b32_e64 v190, v230, 1.0, s[4:5]
	s_waitcnt vmcnt(8)
	v_add_f32_e32 v240, v240, v241
	v_add_f32_e32 v242, v242, v243
	v_add_f32_e32 v240, v240, v242
	v_fmamk_f32 v240, v240, 0x3a800000, v226
	v_rsq_f32_e32 v240, v240
	v_add_f32_e32 v244, v244, v245
	v_add_f32_e32 v184, v184, v189
	v_add_f32_e32 v244, v244, v184
	v_fmamk_f32 v244, v244, 0x3a800000, v226
	v_rsq_f32_e32 v244, v244
	v_and_b32_e32 v191, 15, v185
	v_lshlrev_b32_e32 v191, 2, v191
	v_add_u32_e32 v192, 64, v191
	v_add_u32_e32 v193, 0x80, v191
	v_add_u32_e32 v194, 0xc0, v191
	v_mul_f32_e32 v240, v240, v190
	v_mul_f32_e32 v244, v244, v190
	ds_bpermute_b32 v144, v191, v240
	ds_bpermute_b32 v146, v191, v244
	ds_bpermute_b32 v148, v192, v240
	ds_bpermute_b32 v150, v192, v244
	ds_bpermute_b32 v152, v193, v240
	ds_bpermute_b32 v154, v193, v244
	ds_bpermute_b32 v156, v194, v240
	ds_bpermute_b32 v168, v194, v244
	s_movk_i32 s6, 0x1a00
	v_lshl_or_b32 v170, s52, 8, v187
	v_lshlrev_b32_e32 v170, 1, v170
	v_mov_b32_e32 v171, 0
	v_mov_b64_e32 v[172:173], s[14:15]
	v_mad_i64_i32 v[172:173], s[4:5], v182, s6, v[172:173]
	v_lshl_add_u64 v[172:173], v[172:173], 0, v[170:171]
	s_waitcnt lgkmcnt(0)
	v_pk_mul_f32 v[126:127], v[126:127], v[144:145] op_sel_hi:[1,0]
	v_pk_mul_f32 v[128:129], v[128:129], v[144:145] op_sel_hi:[1,0]
	v_pk_mul_f32 v[122:123], v[122:123], v[144:145] op_sel_hi:[1,0]
	v_pk_mul_f32 v[124:125], v[124:125], v[144:145] op_sel_hi:[1,0]
	v_cvt_pk_bf16_f32 v126, v126, v127
	v_cvt_pk_bf16_f32 v127, v128, v129
	v_cvt_pk_bf16_f32 v128, v122, v123
	v_cvt_pk_bf16_f32 v129, v124, v125
	global_store_dwordx4 v[172:173], v[126:129], off
	v_pk_mul_f32 v[118:119], v[118:119], v[144:145] op_sel_hi:[1,0]
	v_pk_mul_f32 v[120:121], v[120:121], v[144:145] op_sel_hi:[1,0]
	v_pk_mul_f32 v[110:111], v[110:111], v[144:145] op_sel_hi:[1,0]
	v_pk_mul_f32 v[112:113], v[112:113], v[144:145] op_sel_hi:[1,0]
	v_cvt_pk_bf16_f32 v118, v118, v119
	v_cvt_pk_bf16_f32 v119, v120, v121
	v_cvt_pk_bf16_f32 v120, v110, v111
	v_cvt_pk_bf16_f32 v121, v112, v113
	global_store_dwordx4 v[172:173], v[118:121], off offset:256
	s_mov_b64 s[40:41], 0x1a000
	v_lshl_add_u64 v[176:177], v[172:173], 0, s[40:41]
	v_pk_mul_f32 v[114:115], v[114:115], v[146:147] op_sel_hi:[1,0]
	v_pk_mul_f32 v[116:117], v[116:117], v[146:147] op_sel_hi:[1,0]
	v_pk_mul_f32 v[106:107], v[106:107], v[146:147] op_sel_hi:[1,0]
	v_pk_mul_f32 v[108:109], v[108:109], v[146:147] op_sel_hi:[1,0]
	v_cvt_pk_bf16_f32 v114, v114, v115
	v_cvt_pk_bf16_f32 v115, v116, v117
	v_cvt_pk_bf16_f32 v116, v106, v107
	v_cvt_pk_bf16_f32 v117, v108, v109
	global_store_dwordx4 v[176:177], v[114:117], off
	v_pk_mul_f32 v[102:103], v[102:103], v[146:147] op_sel_hi:[1,0]
	v_pk_mul_f32 v[104:105], v[104:105], v[146:147] op_sel_hi:[1,0]
	v_pk_mul_f32 v[94:95], v[94:95], v[146:147] op_sel_hi:[1,0]
	v_pk_mul_f32 v[96:97], v[96:97], v[146:147] op_sel_hi:[1,0]
	v_cvt_pk_bf16_f32 v102, v102, v103
	v_cvt_pk_bf16_f32 v103, v104, v105
	v_cvt_pk_bf16_f32 v104, v94, v95
	v_cvt_pk_bf16_f32 v105, v96, v97
	global_store_dwordx4 v[176:177], v[102:105], off offset:256
	s_and_b64 vcc, exec, s[18:19]
	s_cbranch_vccz .Lalign_e1e
	s_barrier
.Lalign_e1e:
	s_mov_b64 s[40:41], 0x34000
	v_lshl_add_u64 v[174:175], v[172:173], 0, s[40:41]
	v_pk_mul_f32 v[98:99], v[98:99], v[148:149] op_sel_hi:[1,0]
	v_pk_mul_f32 v[100:101], v[100:101], v[148:149] op_sel_hi:[1,0]
	v_pk_mul_f32 v[90:91], v[90:91], v[148:149] op_sel_hi:[1,0]
	v_pk_mul_f32 v[92:93], v[92:93], v[148:149] op_sel_hi:[1,0]
	v_cvt_pk_bf16_f32 v98, v98, v99
	v_cvt_pk_bf16_f32 v99, v100, v101
	v_cvt_pk_bf16_f32 v100, v90, v91
	v_cvt_pk_bf16_f32 v101, v92, v93
	global_store_dwordx4 v[174:175], v[98:101], off
	v_pk_mul_f32 v[86:87], v[86:87], v[148:149] op_sel_hi:[1,0]
	v_pk_mul_f32 v[88:89], v[88:89], v[148:149] op_sel_hi:[1,0]
	v_pk_mul_f32 v[78:79], v[78:79], v[148:149] op_sel_hi:[1,0]
	v_pk_mul_f32 v[80:81], v[80:81], v[148:149] op_sel_hi:[1,0]
	v_cvt_pk_bf16_f32 v86, v86, v87
	v_cvt_pk_bf16_f32 v87, v88, v89
	v_cvt_pk_bf16_f32 v88, v78, v79
	v_cvt_pk_bf16_f32 v89, v80, v81
	global_store_dwordx4 v[174:175], v[86:89], off offset:256
	s_mov_b64 s[40:41], 0x4e000
	v_lshl_add_u64 v[176:177], v[172:173], 0, s[40:41]
	v_pk_mul_f32 v[82:83], v[82:83], v[150:151] op_sel_hi:[1,0]
	v_pk_mul_f32 v[84:85], v[84:85], v[150:151] op_sel_hi:[1,0]
	v_pk_mul_f32 v[74:75], v[74:75], v[150:151] op_sel_hi:[1,0]
	v_pk_mul_f32 v[76:77], v[76:77], v[150:151] op_sel_hi:[1,0]
	v_cvt_pk_bf16_f32 v82, v82, v83
	v_cvt_pk_bf16_f32 v83, v84, v85
	v_cvt_pk_bf16_f32 v84, v74, v75
	v_cvt_pk_bf16_f32 v85, v76, v77
	global_store_dwordx4 v[176:177], v[82:85], off
	v_pk_mul_f32 v[70:71], v[70:71], v[150:151] op_sel_hi:[1,0]
	v_pk_mul_f32 v[72:73], v[72:73], v[150:151] op_sel_hi:[1,0]
	v_pk_mul_f32 v[66:67], v[66:67], v[150:151] op_sel_hi:[1,0]
	v_pk_mul_f32 v[68:69], v[68:69], v[150:151] op_sel_hi:[1,0]
	v_cvt_pk_bf16_f32 v70, v70, v71
	v_cvt_pk_bf16_f32 v71, v72, v73
	v_cvt_pk_bf16_f32 v72, v66, v67
	v_cvt_pk_bf16_f32 v73, v68, v69
	global_store_dwordx4 v[176:177], v[70:73], off offset:256
	s_mov_b64 s[40:41], 0xd0000
	v_lshl_add_u64 v[174:175], v[172:173], 0, s[40:41]
	v_pk_mul_f32 v[62:63], v[62:63], v[152:153] op_sel_hi:[1,0]
	v_pk_mul_f32 v[64:65], v[64:65], v[152:153] op_sel_hi:[1,0]
	v_pk_mul_f32 v[58:59], v[58:59], v[152:153] op_sel_hi:[1,0]
	v_pk_mul_f32 v[60:61], v[60:61], v[152:153] op_sel_hi:[1,0]
	v_cvt_pk_bf16_f32 v62, v62, v63
	v_cvt_pk_bf16_f32 v63, v64, v65
	v_cvt_pk_bf16_f32 v64, v58, v59
	v_cvt_pk_bf16_f32 v65, v60, v61
	global_store_dwordx4 v[174:175], v[62:65], off
	v_pk_mul_f32 v[54:55], v[54:55], v[152:153] op_sel_hi:[1,0]
	v_pk_mul_f32 v[56:57], v[56:57], v[152:153] op_sel_hi:[1,0]
	v_pk_mul_f32 v[46:47], v[46:47], v[152:153] op_sel_hi:[1,0]
	v_pk_mul_f32 v[48:49], v[48:49], v[152:153] op_sel_hi:[1,0]
	v_cvt_pk_bf16_f32 v54, v54, v55
	v_cvt_pk_bf16_f32 v55, v56, v57
	v_cvt_pk_bf16_f32 v56, v46, v47
	v_cvt_pk_bf16_f32 v57, v48, v49
	global_store_dwordx4 v[174:175], v[54:57], off offset:256
	s_mov_b64 s[40:41], 0xea000
	v_lshl_add_u64 v[176:177], v[172:173], 0, s[40:41]
	v_pk_mul_f32 v[50:51], v[50:51], v[154:155] op_sel_hi:[1,0]
	v_pk_mul_f32 v[52:53], v[52:53], v[154:155] op_sel_hi:[1,0]
	v_pk_mul_f32 v[42:43], v[42:43], v[154:155] op_sel_hi:[1,0]
	v_pk_mul_f32 v[44:45], v[44:45], v[154:155] op_sel_hi:[1,0]
	v_cvt_pk_bf16_f32 v50, v50, v51
	v_cvt_pk_bf16_f32 v51, v52, v53
	v_cvt_pk_bf16_f32 v52, v42, v43
	v_cvt_pk_bf16_f32 v53, v44, v45
	global_store_dwordx4 v[176:177], v[50:53], off
	v_pk_mul_f32 v[38:39], v[38:39], v[154:155] op_sel_hi:[1,0]
	v_pk_mul_f32 v[40:41], v[40:41], v[154:155] op_sel_hi:[1,0]
	v_pk_mul_f32 v[30:31], v[30:31], v[154:155] op_sel_hi:[1,0]
	v_pk_mul_f32 v[32:33], v[32:33], v[154:155] op_sel_hi:[1,0]
	v_cvt_pk_bf16_f32 v38, v38, v39
	v_cvt_pk_bf16_f32 v39, v40, v41
	v_cvt_pk_bf16_f32 v40, v30, v31
	v_cvt_pk_bf16_f32 v41, v32, v33
	global_store_dwordx4 v[176:177], v[38:41], off offset:256
	s_mov_b64 s[40:41], 0x104000
	v_lshl_add_u64 v[174:175], v[172:173], 0, s[40:41]
	v_pk_mul_f32 v[34:35], v[34:35], v[156:157] op_sel_hi:[1,0]
	v_pk_mul_f32 v[36:37], v[36:37], v[156:157] op_sel_hi:[1,0]
	v_pk_mul_f32 v[26:27], v[26:27], v[156:157] op_sel_hi:[1,0]
	v_pk_mul_f32 v[28:29], v[28:29], v[156:157] op_sel_hi:[1,0]
	v_cvt_pk_bf16_f32 v34, v34, v35
	v_cvt_pk_bf16_f32 v35, v36, v37
	v_cvt_pk_bf16_f32 v36, v26, v27
	v_cvt_pk_bf16_f32 v37, v28, v29
	global_store_dwordx4 v[174:175], v[34:37], off
	v_pk_mul_f32 v[22:23], v[22:23], v[156:157] op_sel_hi:[1,0]
	v_pk_mul_f32 v[24:25], v[24:25], v[156:157] op_sel_hi:[1,0]
	v_pk_mul_f32 v[14:15], v[14:15], v[156:157] op_sel_hi:[1,0]
	v_pk_mul_f32 v[16:17], v[16:17], v[156:157] op_sel_hi:[1,0]
	v_cvt_pk_bf16_f32 v22, v22, v23
	v_cvt_pk_bf16_f32 v23, v24, v25
	v_cvt_pk_bf16_f32 v24, v14, v15
	v_cvt_pk_bf16_f32 v25, v16, v17
	global_store_dwordx4 v[174:175], v[22:25], off offset:256
	s_mov_b64 s[40:41], 0x11e000
	v_lshl_add_u64 v[176:177], v[172:173], 0, s[40:41]
	v_pk_mul_f32 v[18:19], v[18:19], v[168:169] op_sel_hi:[1,0]
	v_pk_mul_f32 v[20:21], v[20:21], v[168:169] op_sel_hi:[1,0]
	v_pk_mul_f32 v[10:11], v[10:11], v[168:169] op_sel_hi:[1,0]
	v_pk_mul_f32 v[12:13], v[12:13], v[168:169] op_sel_hi:[1,0]
	v_cvt_pk_bf16_f32 v18, v18, v19
	v_cvt_pk_bf16_f32 v19, v20, v21
	v_cvt_pk_bf16_f32 v20, v10, v11
	v_cvt_pk_bf16_f32 v21, v12, v13
	global_store_dwordx4 v[176:177], v[18:21], off
	v_pk_mul_f32 v[6:7], v[6:7], v[168:169] op_sel_hi:[1,0]
	v_pk_mul_f32 v[8:9], v[8:9], v[168:169] op_sel_hi:[1,0]
	v_pk_mul_f32 v[2:3], v[2:3], v[168:169] op_sel_hi:[1,0]
	v_pk_mul_f32 v[4:5], v[4:5], v[168:169] op_sel_hi:[1,0]
	v_cvt_pk_bf16_f32 v6, v6, v7
	v_cvt_pk_bf16_f32 v7, v8, v9
	v_cvt_pk_bf16_f32 v8, v2, v3
	v_cvt_pk_bf16_f32 v9, v4, v5
	global_store_dwordx4 v[176:177], v[6:9], off offset:256
	s_nop 3
	v_mfma_f32_32x32x16_bf16 v[2:17], v[200:203], v[200:203], 0
	v_mfma_f32_32x32x16_bf16 v[18:33], v[200:203], v[200:203], 0
	v_mfma_f32_32x32x16_bf16 v[34:49], v[200:203], v[200:203], 0
	v_mfma_f32_32x32x16_bf16 v[50:65], v[200:203], v[200:203], 0
	v_mfma_f32_32x32x16_bf16 v[66:81], v[200:203], v[200:203], 0
	v_mfma_f32_32x32x16_bf16 v[82:97], v[200:203], v[200:203], 0
	v_mfma_f32_32x32x16_bf16 v[98:113], v[200:203], v[200:203], 0
	v_mfma_f32_32x32x16_bf16 v[114:129], v[200:203], v[200:203], 0
	s_andn2_b64 vcc, exec, s[38:39]
	s_mov_b64 s[6:7], -1
	s_cbranch_vccnz .LBB0_832
	s_andn2_b64 vcc, exec, s[12:13]
	s_cbranch_vccnz .LBB0_831
	s_branch .LBB0_831

.LBB0_2626:
	s_add_u32 s26, s6, 0xfffc0080
	s_addc_u32 s27, s7, -1
	s_add_i32 s50, 0, 0x10000
	s_cmp_eq_u32 s49, 12
	s_cselect_b32 s29, s21, s27
	s_cselect_b32 s28, s33, s26
	s_cselect_b32 s27, s19, s48
	s_cselect_b32 s26, s40, s41
	s_add_i32 s58, 0, 0x14000
	ds_read_b128 v[130:133], v167
	ds_read_b128 v[134:137], v167 offset:1024
	ds_read_b128 v[138:141], v167 offset:2048
	ds_read_b128 v[142:145], v167 offset:3072
	ds_read_b128 v[146:149], v167 offset:16384
	ds_read_b128 v[150:153], v167 offset:17408
	ds_read_b128 v[154:157], v167 offset:18432
	ds_read_b128 v[170:173], v167 offset:19456
	s_add_i32 m0, s36, 0xc000
	ds_read_b128 v[174:177], v183
	ds_read_b128 v[184:187], v183 offset:1024
	ds_read_b128 v[188:191], v183 offset:2048
	ds_read_b128 v[192:195], v183 offset:3072
	ds_read_b128 v[196:199], v183 offset:4096
	ds_read_b128 v[200:203], v183 offset:5120
	ds_read_b128 v[204:207], v183 offset:6144
	global_load_lds_dwordx4 v168, s[6:7]
	s_add_i32 m0, s36, 0xe000
	ds_read_b128 v[216:219], v183 offset:7168
	global_load_lds_dwordx4 v166, s[6:7]
	s_waitcnt vmcnt(8) lgkmcnt(0)
	s_barrier
	v_mfma_f32_16x16x32_bf16 v[126:129], v[130:133], v[174:177], v[126:129]
	v_mfma_f32_16x16x32_bf16 v[122:125], v[138:141], v[174:177], v[122:125]
	v_mfma_f32_16x16x32_bf16 v[110:113], v[130:133], v[188:191], v[110:113]
	v_mfma_f32_16x16x32_bf16 v[106:109], v[138:141], v[188:191], v[106:109]
	v_mfma_f32_16x16x32_bf16 v[94:97], v[130:133], v[196:199], v[94:97]
	v_mfma_f32_16x16x32_bf16 v[90:93], v[138:141], v[196:199], v[90:93]
	v_mfma_f32_16x16x32_bf16 v[78:81], v[130:133], v[204:207], v[78:81]
	v_mfma_f32_16x16x32_bf16 v[74:77], v[138:141], v[204:207], v[74:77]
	v_mfma_f32_16x16x32_bf16 v[126:129], v[134:137], v[184:187], v[126:129]
	v_mfma_f32_16x16x32_bf16 v[122:125], v[142:145], v[184:187], v[122:125]
	v_mfma_f32_16x16x32_bf16 v[110:113], v[134:137], v[192:195], v[110:113]
	v_mfma_f32_16x16x32_bf16 v[106:109], v[142:145], v[192:195], v[106:109]
	v_mfma_f32_16x16x32_bf16 v[94:97], v[134:137], v[200:203], v[94:97]
	v_mfma_f32_16x16x32_bf16 v[90:93], v[142:145], v[200:203], v[90:93]
	v_mfma_f32_16x16x32_bf16 v[78:81], v[134:137], v[216:219], v[78:81]
	v_mfma_f32_16x16x32_bf16 v[74:77], v[142:145], v[216:219], v[74:77]
	v_mfma_f32_16x16x32_bf16 v[118:121], v[146:149], v[174:177], v[118:121]
	v_mfma_f32_16x16x32_bf16 v[114:117], v[154:157], v[174:177], v[114:117]
	v_mfma_f32_16x16x32_bf16 v[102:105], v[146:149], v[188:191], v[102:105]
	v_mfma_f32_16x16x32_bf16 v[98:101], v[154:157], v[188:191], v[98:101]
	v_mfma_f32_16x16x32_bf16 v[86:89], v[146:149], v[196:199], v[86:89]
	v_mfma_f32_16x16x32_bf16 v[82:85], v[154:157], v[196:199], v[82:85]
	v_mfma_f32_16x16x32_bf16 v[70:73], v[146:149], v[204:207], v[70:73]
	v_mfma_f32_16x16x32_bf16 v[66:69], v[154:157], v[204:207], v[66:69]
	v_mfma_f32_16x16x32_bf16 v[118:121], v[150:153], v[184:187], v[118:121]
	v_mfma_f32_16x16x32_bf16 v[114:117], v[170:173], v[184:187], v[114:117]
	v_mfma_f32_16x16x32_bf16 v[102:105], v[150:153], v[192:195], v[102:105]
	v_mfma_f32_16x16x32_bf16 v[98:101], v[170:173], v[192:195], v[98:101]
	v_mfma_f32_16x16x32_bf16 v[86:89], v[150:153], v[200:203], v[86:89]
	v_mfma_f32_16x16x32_bf16 v[82:85], v[170:173], v[200:203], v[82:85]
	v_mfma_f32_16x16x32_bf16 v[70:73], v[150:153], v[216:219], v[70:73]
	v_mfma_f32_16x16x32_bf16 v[66:69], v[170:173], v[216:219], v[66:69]
	s_barrier
	s_add_i32 s50, s50, s35
	v_lshl_add_u64 v[178:179], s[26:27], 0, v[162:163]
	s_mov_b32 m0, s50
	ds_read_b128 v[174:177], v183 offset:16384
	ds_read_b128 v[184:187], v183 offset:17408
	ds_read_b128 v[188:191], v183 offset:18432
	ds_read_b128 v[192:195], v183 offset:19456
	ds_read_b128 v[196:199], v183 offset:20480
	ds_read_b128 v[200:203], v183 offset:21504
	ds_read_b128 v[204:207], v183 offset:22528
	ds_read_b128 v[216:219], v183 offset:23552
	global_load_lds_dwordx4 v162, s[26:27]
	s_add_i32 m0, s50, 0x2000
	s_add_u32 s52, s26, 0x40000
	v_lshl_add_u64 v[208:209], s[26:27], 0, v[158:159]
	s_addc_u32 s53, s27, 0
	s_add_i32 s50, s58, s35
	global_load_lds_dwordx4 v158, s[26:27]
	s_mov_b32 m0, s50
	v_lshl_add_u64 v[222:223], s[28:29], 0, v[160:161]
	global_load_lds_dwordx4 v162, s[52:53]
	s_add_i32 m0, s50, 0x2000
	s_nop 0
	global_load_lds_dwordx4 v158, s[52:53]
	s_mov_b32 m0, s36
	v_lshl_add_u64 v[220:221], s[28:29], 0, v[164:165]
	global_load_lds_dwordx4 v164, s[28:29]
	s_mov_b32 m0, s37
	s_nop 0
	global_load_lds_dwordx4 v160, s[28:29]
	s_waitcnt vmcnt(8) lgkmcnt(0)
	s_barrier
	v_mfma_f32_16x16x32_bf16 v[62:65], v[130:133], v[174:177], v[62:65]
	v_mfma_f32_16x16x32_bf16 v[58:61], v[138:141], v[174:177], v[58:61]
	v_mfma_f32_16x16x32_bf16 v[46:49], v[130:133], v[188:191], v[46:49]
	v_mfma_f32_16x16x32_bf16 v[42:45], v[138:141], v[188:191], v[42:45]
	v_mfma_f32_16x16x32_bf16 v[30:33], v[130:133], v[196:199], v[30:33]
	v_mfma_f32_16x16x32_bf16 v[26:29], v[138:141], v[196:199], v[26:29]
	v_mfma_f32_16x16x32_bf16 v[14:17], v[130:133], v[204:207], v[14:17]
	v_mfma_f32_16x16x32_bf16 v[10:13], v[138:141], v[204:207], v[10:13]
	v_mfma_f32_16x16x32_bf16 v[62:65], v[134:137], v[184:187], v[62:65]
	v_mfma_f32_16x16x32_bf16 v[58:61], v[142:145], v[184:187], v[58:61]
	v_mfma_f32_16x16x32_bf16 v[46:49], v[134:137], v[192:195], v[46:49]
	v_mfma_f32_16x16x32_bf16 v[42:45], v[142:145], v[192:195], v[42:45]
	v_mfma_f32_16x16x32_bf16 v[30:33], v[134:137], v[200:203], v[30:33]
	v_mfma_f32_16x16x32_bf16 v[26:29], v[142:145], v[200:203], v[26:29]
	v_mfma_f32_16x16x32_bf16 v[14:17], v[134:137], v[216:219], v[14:17]
	v_mfma_f32_16x16x32_bf16 v[10:13], v[142:145], v[216:219], v[10:13]
	v_mfma_f32_16x16x32_bf16 v[54:57], v[146:149], v[174:177], v[54:57]
	v_mfma_f32_16x16x32_bf16 v[50:53], v[154:157], v[174:177], v[50:53]
	v_mfma_f32_16x16x32_bf16 v[38:41], v[146:149], v[188:191], v[38:41]
	v_mfma_f32_16x16x32_bf16 v[34:37], v[154:157], v[188:191], v[34:37]
	v_mfma_f32_16x16x32_bf16 v[22:25], v[146:149], v[196:199], v[22:25]
	v_mfma_f32_16x16x32_bf16 v[18:21], v[154:157], v[196:199], v[18:21]
	v_mfma_f32_16x16x32_bf16 v[6:9], v[146:149], v[204:207], v[6:9]
	v_mfma_f32_16x16x32_bf16 v[2:5], v[154:157], v[204:207], v[2:5]
	v_mfma_f32_16x16x32_bf16 v[54:57], v[150:153], v[184:187], v[54:57]
	v_mfma_f32_16x16x32_bf16 v[50:53], v[170:173], v[184:187], v[50:53]
	v_mfma_f32_16x16x32_bf16 v[38:41], v[150:153], v[192:195], v[38:41]
	v_mfma_f32_16x16x32_bf16 v[34:37], v[170:173], v[192:195], v[34:37]
	v_mfma_f32_16x16x32_bf16 v[22:25], v[150:153], v[200:203], v[22:25]
	v_mfma_f32_16x16x32_bf16 v[18:21], v[170:173], v[200:203], v[18:21]
	v_mfma_f32_16x16x32_bf16 v[6:9], v[150:153], v[216:219], v[6:9]
	v_mfma_f32_16x16x32_bf16 v[2:5], v[170:173], v[216:219], v[2:5]
	s_barrier
	s_add_i32 s50, 0, 0x18000
	s_add_i32 s52, 0, 0x1c000
	ds_read_b128 v[130:133], v167 offset:32768
	ds_read_b128 v[134:137], v167 offset:33792
	ds_read_b128 v[138:141], v167 offset:34816
	ds_read_b128 v[142:145], v167 offset:35840
	ds_read_b128 v[146:149], v167 offset:49152
	ds_read_b128 v[150:153], v167 offset:50176
	ds_read_b128 v[154:157], v167 offset:51200
	ds_read_b128 v[170:173], v167 offset:52224
	s_add_u32 s28, s28, 0x40000
	s_addc_u32 s29, s29, 0
	s_mov_b32 m0, s42
	ds_read_b128 v[174:177], v183 offset:32768
	ds_read_b128 v[184:187], v183 offset:33792
	ds_read_b128 v[188:191], v183 offset:34816
	ds_read_b128 v[192:195], v183 offset:35840
	ds_read_b128 v[196:199], v183 offset:36864
	ds_read_b128 v[200:203], v183 offset:37888
	ds_read_b128 v[204:207], v183 offset:38912
	global_load_lds_dwordx4 v164, s[28:29]
	s_mov_b32 m0, s43
	ds_read_b128 v[216:219], v183 offset:39936
	global_load_lds_dwordx4 v160, s[28:29]
	s_waitcnt vmcnt(8) lgkmcnt(0)
	s_barrier
	v_mfma_f32_16x16x32_bf16 v[126:129], v[130:133], v[174:177], v[126:129]
	v_mfma_f32_16x16x32_bf16 v[122:125], v[138:141], v[174:177], v[122:125]
	v_mfma_f32_16x16x32_bf16 v[110:113], v[130:133], v[188:191], v[110:113]
	v_mfma_f32_16x16x32_bf16 v[106:109], v[138:141], v[188:191], v[106:109]
	v_mfma_f32_16x16x32_bf16 v[94:97], v[130:133], v[196:199], v[94:97]
	v_mfma_f32_16x16x32_bf16 v[90:93], v[138:141], v[196:199], v[90:93]
	v_mfma_f32_16x16x32_bf16 v[78:81], v[130:133], v[204:207], v[78:81]
	v_mfma_f32_16x16x32_bf16 v[74:77], v[138:141], v[204:207], v[74:77]
	v_mfma_f32_16x16x32_bf16 v[126:129], v[134:137], v[184:187], v[126:129]
	v_mfma_f32_16x16x32_bf16 v[122:125], v[142:145], v[184:187], v[122:125]
	v_mfma_f32_16x16x32_bf16 v[110:113], v[134:137], v[192:195], v[110:113]
	v_mfma_f32_16x16x32_bf16 v[106:109], v[142:145], v[192:195], v[106:109]
	v_mfma_f32_16x16x32_bf16 v[94:97], v[134:137], v[200:203], v[94:97]
	v_mfma_f32_16x16x32_bf16 v[90:93], v[142:145], v[200:203], v[90:93]
	v_mfma_f32_16x16x32_bf16 v[78:81], v[134:137], v[216:219], v[78:81]
	v_mfma_f32_16x16x32_bf16 v[74:77], v[142:145], v[216:219], v[74:77]
	v_mfma_f32_16x16x32_bf16 v[118:121], v[146:149], v[174:177], v[118:121]
	v_mfma_f32_16x16x32_bf16 v[114:117], v[154:157], v[174:177], v[114:117]
	v_mfma_f32_16x16x32_bf16 v[102:105], v[146:149], v[188:191], v[102:105]
	v_mfma_f32_16x16x32_bf16 v[98:101], v[154:157], v[188:191], v[98:101]
	v_mfma_f32_16x16x32_bf16 v[86:89], v[146:149], v[196:199], v[86:89]
	v_mfma_f32_16x16x32_bf16 v[82:85], v[154:157], v[196:199], v[82:85]
	v_mfma_f32_16x16x32_bf16 v[70:73], v[146:149], v[204:207], v[70:73]
	v_mfma_f32_16x16x32_bf16 v[66:69], v[154:157], v[204:207], v[66:69]
	v_mfma_f32_16x16x32_bf16 v[118:121], v[150:153], v[184:187], v[118:121]
	v_mfma_f32_16x16x32_bf16 v[114:117], v[170:173], v[184:187], v[114:117]
	v_mfma_f32_16x16x32_bf16 v[102:105], v[150:153], v[192:195], v[102:105]
	v_mfma_f32_16x16x32_bf16 v[98:101], v[170:173], v[192:195], v[98:101]
	v_mfma_f32_16x16x32_bf16 v[86:89], v[150:153], v[200:203], v[86:89]
	v_mfma_f32_16x16x32_bf16 v[82:85], v[170:173], v[200:203], v[82:85]
	v_mfma_f32_16x16x32_bf16 v[70:73], v[150:153], v[216:219], v[70:73]
	v_mfma_f32_16x16x32_bf16 v[66:69], v[170:173], v[216:219], v[66:69]
	s_barrier
	s_add_i32 s28, s50, s35
	v_lshl_add_u64 v[178:179], v[178:179], 0, s[56:57]
	s_mov_b32 m0, s28
	ds_read_b128 v[174:177], v183 offset:49152
	ds_read_b128 v[184:187], v183 offset:50176
	ds_read_b128 v[188:191], v183 offset:51200
	ds_read_b128 v[192:195], v183 offset:52224
	ds_read_b128 v[196:199], v183 offset:53248
	ds_read_b128 v[200:203], v183 offset:54272
	ds_read_b128 v[204:207], v183 offset:55296
	ds_read_b128 v[216:219], v183 offset:56320
	global_load_lds_dwordx4 v[178:179], off
	s_add_i32 m0, s28, 0x2000
	s_add_u32 s26, s26, 0x40080
	v_lshl_add_u64 v[178:179], v[208:209], 0, s[56:57]
	s_addc_u32 s27, s27, 0
	s_add_i32 s28, s52, s35
	global_load_lds_dwordx4 v[178:179], off
	s_mov_b32 m0, s28
	s_nop 0
	global_load_lds_dwordx4 v162, s[26:27]
	s_add_i32 m0, s28, 0x2000
	s_nop 0
	global_load_lds_dwordx4 v158, s[26:27]
	s_mov_b32 m0, s44
	v_lshl_add_u64 v[178:179], v[220:221], 0, s[56:57]
	global_load_lds_dwordx4 v[178:179], off
	s_mov_b32 m0, s45
	v_lshl_add_u64 v[178:179], v[222:223], 0, s[56:57]
	global_load_lds_dwordx4 v[178:179], off
	s_waitcnt vmcnt(8) lgkmcnt(0)
	s_barrier
	v_mfma_f32_16x16x32_bf16 v[62:65], v[130:133], v[174:177], v[62:65]
	v_mfma_f32_16x16x32_bf16 v[58:61], v[138:141], v[174:177], v[58:61]
	v_mfma_f32_16x16x32_bf16 v[46:49], v[130:133], v[188:191], v[46:49]
	v_mfma_f32_16x16x32_bf16 v[42:45], v[138:141], v[188:191], v[42:45]
	v_mfma_f32_16x16x32_bf16 v[30:33], v[130:133], v[196:199], v[30:33]
	v_mfma_f32_16x16x32_bf16 v[26:29], v[138:141], v[196:199], v[26:29]
	v_mfma_f32_16x16x32_bf16 v[14:17], v[130:133], v[204:207], v[14:17]
	v_mfma_f32_16x16x32_bf16 v[10:13], v[138:141], v[204:207], v[10:13]
	v_mfma_f32_16x16x32_bf16 v[62:65], v[134:137], v[184:187], v[62:65]
	v_mfma_f32_16x16x32_bf16 v[58:61], v[142:145], v[184:187], v[58:61]
	v_mfma_f32_16x16x32_bf16 v[46:49], v[134:137], v[192:195], v[46:49]
	v_mfma_f32_16x16x32_bf16 v[42:45], v[142:145], v[192:195], v[42:45]
	v_mfma_f32_16x16x32_bf16 v[30:33], v[134:137], v[200:203], v[30:33]
	v_mfma_f32_16x16x32_bf16 v[26:29], v[142:145], v[200:203], v[26:29]
	v_mfma_f32_16x16x32_bf16 v[14:17], v[134:137], v[216:219], v[14:17]
	v_mfma_f32_16x16x32_bf16 v[10:13], v[142:145], v[216:219], v[10:13]
	v_mfma_f32_16x16x32_bf16 v[54:57], v[146:149], v[174:177], v[54:57]
	v_mfma_f32_16x16x32_bf16 v[50:53], v[154:157], v[174:177], v[50:53]
	v_mfma_f32_16x16x32_bf16 v[38:41], v[146:149], v[188:191], v[38:41]
	v_mfma_f32_16x16x32_bf16 v[34:37], v[154:157], v[188:191], v[34:37]
	v_mfma_f32_16x16x32_bf16 v[22:25], v[146:149], v[196:199], v[22:25]
	v_mfma_f32_16x16x32_bf16 v[18:21], v[154:157], v[196:199], v[18:21]
	v_mfma_f32_16x16x32_bf16 v[6:9], v[146:149], v[204:207], v[6:9]
	v_mfma_f32_16x16x32_bf16 v[2:5], v[154:157], v[204:207], v[2:5]
	v_mfma_f32_16x16x32_bf16 v[54:57], v[150:153], v[184:187], v[54:57]
	v_mfma_f32_16x16x32_bf16 v[50:53], v[170:173], v[184:187], v[50:53]
	v_mfma_f32_16x16x32_bf16 v[38:41], v[150:153], v[192:195], v[38:41]
	v_mfma_f32_16x16x32_bf16 v[34:37], v[170:173], v[192:195], v[34:37]
	v_mfma_f32_16x16x32_bf16 v[22:25], v[150:153], v[200:203], v[22:25]
	v_mfma_f32_16x16x32_bf16 v[18:21], v[170:173], v[200:203], v[18:21]
	v_mfma_f32_16x16x32_bf16 v[6:9], v[150:153], v[216:219], v[6:9]
	v_mfma_f32_16x16x32_bf16 v[2:5], v[170:173], v[216:219], v[2:5]
	s_barrier
	s_add_i32 s49, s49, 2
	s_add_u32 s41, s41, 0x100
	s_addc_u32 s48, s48, 0
	s_add_u32 s6, s6, 0x100
	s_addc_u32 s7, s7, 0
	s_cmp_gt_u32 s49, 13
	s_cbranch_scc0 .LBB0_2626


.LBB0_2629:
	v_mov_b32_e32 v204, 0
	v_mov_b32_e32 v205, 0
	v_mov_b32_e32 v206, 0
	v_mov_b32_e32 v207, 0
	v_lshl_add_u32 v178, s4, 8, v180
	v_and_b32_e32 v130, 8, v182
	v_and_b32_e32 v131, 16, v182
	v_lshlrev_b32_e32 v130, 2, v130
	v_lshl_add_u32 v130, v131, 3, v130
	v_add_u32_e32 v130, v130, v178
	v_mov_b32_e32 v131, 0
	v_lshl_add_u64 v[130:131], v[130:131], 4, s[14:15]
	global_load_dword v140, v[130:131], off offset:268
	s_waitcnt vmcnt(9)
	v_add_f32_e32 v240, v240, v241
	v_add_f32_e32 v242, v242, v243
	v_add_f32_e32 v240, v240, v242
	v_fmamk_f32 v240, v240, 0x3a800000, v226
	v_rsq_f32_e32 v240, v240
	v_and_b32_e32 v190, 15, v180
	v_lshlrev_b32_e32 v190, 2, v190
	v_add_u32_e32 v191, 64, v190
	v_add_u32_e32 v192, 0x80, v190
	v_add_u32_e32 v193, 0xc0, v190
	ds_bpermute_b32 v144, v190, v240
	ds_bpermute_b32 v148, v191, v240
	ds_bpermute_b32 v152, v192, v240
	ds_bpermute_b32 v156, v193, v240
	v_lshl_or_b32 v170, s47, 8, v182
	v_lshlrev_b32_e32 v170, 1, v170
	v_mov_b32_e32 v171, 0
	v_mov_b32_e32 v179, 0
	v_lshlrev_b64 v[172:173], 13, v[178:179]
	v_lshl_add_u64 v[172:173], s[12:13], 0, v[172:173]
	v_lshl_add_u64 v[172:173], v[172:173], 0, v[170:171]
	s_waitcnt lgkmcnt(0)
	v_pk_mul_f32 v[126:127], v[126:127], v[144:145] op_sel_hi:[1,0]
	v_pk_mul_f32 v[128:129], v[128:129], v[144:145] op_sel_hi:[1,0]
	v_pk_mul_f32 v[122:123], v[122:123], v[144:145] op_sel_hi:[1,0]
	v_pk_mul_f32 v[124:125], v[124:125], v[144:145] op_sel_hi:[1,0]
	v_max_f32_e32 v132, 0, v126
	v_max_f32_e32 v133, 0, v127
	v_max_f32_e32 v134, 0, v128
	v_max_f32_e32 v135, 0, v129
	v_max_f32_e32 v136, 0, v122
	v_max_f32_e32 v137, 0, v123
	v_max_f32_e32 v138, 0, v124
	v_max_f32_e32 v139, 0, v125
	v_pk_mul_f32 v[126:127], v[126:127], v[132:133]
	v_pk_mul_f32 v[128:129], v[128:129], v[134:135]
	v_pk_mul_f32 v[122:123], v[122:123], v[136:137]
	v_pk_mul_f32 v[124:125], v[124:125], v[138:139]
	v_cvt_pk_bf16_f32 v126, v126, v127
	v_cvt_pk_bf16_f32 v127, v128, v129
	v_cvt_pk_bf16_f32 v128, v122, v123
	v_cvt_pk_bf16_f32 v129, v124, v125
	global_store_dwordx4 v[172:173], v[126:129], off
	v_pk_mul_f32 v[118:119], v[118:119], v[144:145] op_sel_hi:[1,0]
	v_pk_mul_f32 v[120:121], v[120:121], v[144:145] op_sel_hi:[1,0]
	v_pk_mul_f32 v[114:115], v[114:115], v[144:145] op_sel_hi:[1,0]
	v_pk_mul_f32 v[116:117], v[116:117], v[144:145] op_sel_hi:[1,0]
	v_max_f32_e32 v132, 0, v118
	v_max_f32_e32 v133, 0, v119
	v_max_f32_e32 v134, 0, v120
	v_max_f32_e32 v135, 0, v121
	v_max_f32_e32 v136, 0, v114
	v_max_f32_e32 v137, 0, v115
	v_max_f32_e32 v138, 0, v116
	v_max_f32_e32 v139, 0, v117
	v_pk_mul_f32 v[118:119], v[118:119], v[132:133]
	v_pk_mul_f32 v[120:121], v[120:121], v[134:135]
	v_pk_mul_f32 v[114:115], v[114:115], v[136:137]
	v_pk_mul_f32 v[116:117], v[116:117], v[138:139]
	v_cvt_pk_bf16_f32 v118, v118, v119
	v_cvt_pk_bf16_f32 v119, v120, v121
	v_cvt_pk_bf16_f32 v120, v114, v115
	v_cvt_pk_bf16_f32 v121, v116, v117
	global_store_dwordx4 v[172:173], v[118:121], off offset:256
	s_mov_b64 s[40:41], 0x40000
	v_lshl_add_u64 v[176:177], v[172:173], 0, s[40:41]
	v_pk_mul_f32 v[94:95], v[94:95], v[148:149] op_sel_hi:[1,0]
	v_pk_mul_f32 v[96:97], v[96:97], v[148:149] op_sel_hi:[1,0]
	v_pk_mul_f32 v[90:91], v[90:91], v[148:149] op_sel_hi:[1,0]
	v_pk_mul_f32 v[92:93], v[92:93], v[148:149] op_sel_hi:[1,0]
	v_max_f32_e32 v132, 0, v94
	v_max_f32_e32 v133, 0, v95
	v_max_f32_e32 v134, 0, v96
	v_max_f32_e32 v135, 0, v97
	v_max_f32_e32 v136, 0, v90
	v_max_f32_e32 v137, 0, v91
	v_max_f32_e32 v138, 0, v92
	v_max_f32_e32 v139, 0, v93
	v_pk_mul_f32 v[94:95], v[94:95], v[132:133]
	v_pk_mul_f32 v[96:97], v[96:97], v[134:135]
	v_pk_mul_f32 v[90:91], v[90:91], v[136:137]
	v_pk_mul_f32 v[92:93], v[92:93], v[138:139]
	v_cvt_pk_bf16_f32 v94, v94, v95
	v_cvt_pk_bf16_f32 v95, v96, v97
	v_cvt_pk_bf16_f32 v96, v90, v91
	v_cvt_pk_bf16_f32 v97, v92, v93
	global_store_dwordx4 v[176:177], v[94:97], off
	v_pk_mul_f32 v[86:87], v[86:87], v[148:149] op_sel_hi:[1,0]
	v_pk_mul_f32 v[88:89], v[88:89], v[148:149] op_sel_hi:[1,0]
	v_pk_mul_f32 v[82:83], v[82:83], v[148:149] op_sel_hi:[1,0]
	v_pk_mul_f32 v[84:85], v[84:85], v[148:149] op_sel_hi:[1,0]
	v_max_f32_e32 v132, 0, v86
	v_max_f32_e32 v133, 0, v87
	v_max_f32_e32 v134, 0, v88
	v_max_f32_e32 v135, 0, v89
	v_max_f32_e32 v136, 0, v82
	v_max_f32_e32 v137, 0, v83
	v_max_f32_e32 v138, 0, v84
	v_max_f32_e32 v139, 0, v85
	v_pk_mul_f32 v[86:87], v[86:87], v[132:133]
	v_pk_mul_f32 v[88:89], v[88:89], v[134:135]
	v_pk_mul_f32 v[82:83], v[82:83], v[136:137]
	v_pk_mul_f32 v[84:85], v[84:85], v[138:139]
	v_cvt_pk_bf16_f32 v86, v86, v87
	v_cvt_pk_bf16_f32 v87, v88, v89
	v_cvt_pk_bf16_f32 v88, v82, v83
	v_cvt_pk_bf16_f32 v89, v84, v85
	global_store_dwordx4 v[176:177], v[86:89], off offset:256
	s_and_b64 vcc, exec, s[16:17]
	s_cbranch_vccz .Lalign_c6
	s_barrier
.Lalign_c6:
	s_mov_b64 s[40:41], 0x100000
	v_lshl_add_u64 v[174:175], v[172:173], 0, s[40:41]
	v_pk_mul_f32 v[62:63], v[62:63], v[152:153] op_sel_hi:[1,0]
	v_pk_mul_f32 v[64:65], v[64:65], v[152:153] op_sel_hi:[1,0]
	v_pk_mul_f32 v[58:59], v[58:59], v[152:153] op_sel_hi:[1,0]
	v_pk_mul_f32 v[60:61], v[60:61], v[152:153] op_sel_hi:[1,0]
	v_max_f32_e32 v132, 0, v62
	v_max_f32_e32 v133, 0, v63
	v_max_f32_e32 v134, 0, v64
	v_max_f32_e32 v135, 0, v65
	v_max_f32_e32 v136, 0, v58
	v_max_f32_e32 v137, 0, v59
	v_max_f32_e32 v138, 0, v60
	v_max_f32_e32 v139, 0, v61
	v_pk_mul_f32 v[62:63], v[62:63], v[132:133]
	v_pk_mul_f32 v[64:65], v[64:65], v[134:135]
	v_pk_mul_f32 v[58:59], v[58:59], v[136:137]
	v_pk_mul_f32 v[60:61], v[60:61], v[138:139]
	v_cvt_pk_bf16_f32 v62, v62, v63
	v_cvt_pk_bf16_f32 v63, v64, v65
	v_cvt_pk_bf16_f32 v64, v58, v59
	v_cvt_pk_bf16_f32 v65, v60, v61
	global_store_dwordx4 v[174:175], v[62:65], off
	v_pk_mul_f32 v[54:55], v[54:55], v[152:153] op_sel_hi:[1,0]
	v_pk_mul_f32 v[56:57], v[56:57], v[152:153] op_sel_hi:[1,0]
	v_pk_mul_f32 v[50:51], v[50:51], v[152:153] op_sel_hi:[1,0]
	v_pk_mul_f32 v[52:53], v[52:53], v[152:153] op_sel_hi:[1,0]
	v_max_f32_e32 v132, 0, v54
	v_max_f32_e32 v133, 0, v55
	v_max_f32_e32 v134, 0, v56
	v_max_f32_e32 v135, 0, v57
	v_max_f32_e32 v136, 0, v50
	v_max_f32_e32 v137, 0, v51
	v_max_f32_e32 v138, 0, v52
	v_max_f32_e32 v139, 0, v53
	v_pk_mul_f32 v[54:55], v[54:55], v[132:133]
	v_pk_mul_f32 v[56:57], v[56:57], v[134:135]
	v_pk_mul_f32 v[50:51], v[50:51], v[136:137]
	v_pk_mul_f32 v[52:53], v[52:53], v[138:139]
	v_cvt_pk_bf16_f32 v54, v54, v55
	v_cvt_pk_bf16_f32 v55, v56, v57
	v_cvt_pk_bf16_f32 v56, v50, v51
	v_cvt_pk_bf16_f32 v57, v52, v53
	global_store_dwordx4 v[174:175], v[54:57], off offset:256
	s_mov_b64 s[40:41], 0x140000
	v_lshl_add_u64 v[176:177], v[172:173], 0, s[40:41]
	v_pk_mul_f32 v[30:31], v[30:31], v[156:157] op_sel_hi:[1,0]
	v_pk_mul_f32 v[32:33], v[32:33], v[156:157] op_sel_hi:[1,0]
	v_pk_mul_f32 v[26:27], v[26:27], v[156:157] op_sel_hi:[1,0]
	v_pk_mul_f32 v[28:29], v[28:29], v[156:157] op_sel_hi:[1,0]
	v_max_f32_e32 v132, 0, v30
	v_max_f32_e32 v133, 0, v31
	v_max_f32_e32 v134, 0, v32
	v_max_f32_e32 v135, 0, v33
	v_max_f32_e32 v136, 0, v26
	v_max_f32_e32 v137, 0, v27
	v_max_f32_e32 v138, 0, v28
	v_max_f32_e32 v139, 0, v29
	v_pk_mul_f32 v[30:31], v[30:31], v[132:133]
	v_pk_mul_f32 v[32:33], v[32:33], v[134:135]
	v_pk_mul_f32 v[26:27], v[26:27], v[136:137]
	v_pk_mul_f32 v[28:29], v[28:29], v[138:139]
	v_cvt_pk_bf16_f32 v30, v30, v31
	v_cvt_pk_bf16_f32 v31, v32, v33
	v_cvt_pk_bf16_f32 v32, v26, v27
	v_cvt_pk_bf16_f32 v33, v28, v29
	global_store_dwordx4 v[176:177], v[30:33], off
	v_pk_mul_f32 v[22:23], v[22:23], v[156:157] op_sel_hi:[1,0]
	v_pk_mul_f32 v[24:25], v[24:25], v[156:157] op_sel_hi:[1,0]
	v_pk_mul_f32 v[18:19], v[18:19], v[156:157] op_sel_hi:[1,0]
	v_pk_mul_f32 v[20:21], v[20:21], v[156:157] op_sel_hi:[1,0]
	v_max_f32_e32 v132, 0, v22
	v_max_f32_e32 v133, 0, v23
	v_max_f32_e32 v134, 0, v24
	v_max_f32_e32 v135, 0, v25
	v_max_f32_e32 v136, 0, v18
	v_max_f32_e32 v137, 0, v19
	v_max_f32_e32 v138, 0, v20
	v_max_f32_e32 v139, 0, v21
	v_pk_mul_f32 v[22:23], v[22:23], v[132:133]
	v_pk_mul_f32 v[24:25], v[24:25], v[134:135]
	v_pk_mul_f32 v[18:19], v[18:19], v[136:137]
	v_pk_mul_f32 v[20:21], v[20:21], v[138:139]
	v_cvt_pk_bf16_f32 v22, v22, v23
	v_cvt_pk_bf16_f32 v23, v24, v25
	v_cvt_pk_bf16_f32 v24, v18, v19
	v_cvt_pk_bf16_f32 v25, v20, v21
	global_store_dwordx4 v[176:177], v[22:25], off offset:256
	s_waitcnt vmcnt(8)
	v_add_f32_e32 v244, v244, v245
	v_add_f32_e32 v239, v239, v140
	v_add_f32_e32 v244, v244, v239
	v_fmamk_f32 v244, v244, 0x3a800000, v226
	v_rsq_f32_e32 v244, v244
	s_nop 0
	ds_bpermute_b32 v146, v190, v244
	ds_bpermute_b32 v150, v191, v244
	ds_bpermute_b32 v154, v192, v244
	ds_bpermute_b32 v194, v193, v244
	s_waitcnt lgkmcnt(0)
	s_mov_b64 s[40:41], 0x20000
	v_lshl_add_u64 v[174:175], v[172:173], 0, s[40:41]
	v_pk_mul_f32 v[110:111], v[110:111], v[146:147] op_sel_hi:[1,0]
	v_pk_mul_f32 v[112:113], v[112:113], v[146:147] op_sel_hi:[1,0]
	v_pk_mul_f32 v[106:107], v[106:107], v[146:147] op_sel_hi:[1,0]
	v_pk_mul_f32 v[108:109], v[108:109], v[146:147] op_sel_hi:[1,0]
	v_max_f32_e32 v132, 0, v110
	v_max_f32_e32 v133, 0, v111
	v_max_f32_e32 v134, 0, v112
	v_max_f32_e32 v135, 0, v113
	v_max_f32_e32 v136, 0, v106
	v_max_f32_e32 v137, 0, v107
	v_max_f32_e32 v138, 0, v108
	v_max_f32_e32 v139, 0, v109
	v_pk_mul_f32 v[110:111], v[110:111], v[132:133]
	v_pk_mul_f32 v[112:113], v[112:113], v[134:135]
	v_pk_mul_f32 v[106:107], v[106:107], v[136:137]
	v_pk_mul_f32 v[108:109], v[108:109], v[138:139]
	v_cvt_pk_bf16_f32 v110, v110, v111
	v_cvt_pk_bf16_f32 v111, v112, v113
	v_cvt_pk_bf16_f32 v112, v106, v107
	v_cvt_pk_bf16_f32 v113, v108, v109
	global_store_dwordx4 v[174:175], v[110:113], off
	v_pk_mul_f32 v[102:103], v[102:103], v[146:147] op_sel_hi:[1,0]
	v_pk_mul_f32 v[104:105], v[104:105], v[146:147] op_sel_hi:[1,0]
	v_pk_mul_f32 v[98:99], v[98:99], v[146:147] op_sel_hi:[1,0]
	v_pk_mul_f32 v[100:101], v[100:101], v[146:147] op_sel_hi:[1,0]
	v_max_f32_e32 v132, 0, v102
	v_max_f32_e32 v133, 0, v103
	v_max_f32_e32 v134, 0, v104
	v_max_f32_e32 v135, 0, v105
	v_max_f32_e32 v136, 0, v98
	v_max_f32_e32 v137, 0, v99
	v_max_f32_e32 v138, 0, v100
	v_max_f32_e32 v139, 0, v101
	v_pk_mul_f32 v[102:103], v[102:103], v[132:133]
	v_pk_mul_f32 v[104:105], v[104:105], v[134:135]
	v_pk_mul_f32 v[98:99], v[98:99], v[136:137]
	v_pk_mul_f32 v[100:101], v[100:101], v[138:139]
	v_cvt_pk_bf16_f32 v102, v102, v103
	v_cvt_pk_bf16_f32 v103, v104, v105
	v_cvt_pk_bf16_f32 v104, v98, v99
	v_cvt_pk_bf16_f32 v105, v100, v101
	global_store_dwordx4 v[174:175], v[102:105], off offset:256
	s_mov_b64 s[40:41], 0x60000
	v_lshl_add_u64 v[176:177], v[172:173], 0, s[40:41]
	v_pk_mul_f32 v[78:79], v[78:79], v[150:151] op_sel_hi:[1,0]
	v_pk_mul_f32 v[80:81], v[80:81], v[150:151] op_sel_hi:[1,0]
	v_pk_mul_f32 v[74:75], v[74:75], v[150:151] op_sel_hi:[1,0]
	v_pk_mul_f32 v[76:77], v[76:77], v[150:151] op_sel_hi:[1,0]
	v_max_f32_e32 v132, 0, v78
	v_max_f32_e32 v133, 0, v79
	v_max_f32_e32 v134, 0, v80
	v_max_f32_e32 v135, 0, v81
	v_max_f32_e32 v136, 0, v74
	v_max_f32_e32 v137, 0, v75
	v_max_f32_e32 v138, 0, v76
	v_max_f32_e32 v139, 0, v77
	v_pk_mul_f32 v[78:79], v[78:79], v[132:133]
	v_pk_mul_f32 v[80:81], v[80:81], v[134:135]
	v_pk_mul_f32 v[74:75], v[74:75], v[136:137]
	v_pk_mul_f32 v[76:77], v[76:77], v[138:139]
	v_cvt_pk_bf16_f32 v78, v78, v79
	v_cvt_pk_bf16_f32 v79, v80, v81
	v_cvt_pk_bf16_f32 v80, v74, v75
	v_cvt_pk_bf16_f32 v81, v76, v77
	global_store_dwordx4 v[176:177], v[78:81], off
	v_pk_mul_f32 v[70:71], v[70:71], v[150:151] op_sel_hi:[1,0]
	v_pk_mul_f32 v[72:73], v[72:73], v[150:151] op_sel_hi:[1,0]
	v_pk_mul_f32 v[66:67], v[66:67], v[150:151] op_sel_hi:[1,0]
	v_pk_mul_f32 v[68:69], v[68:69], v[150:151] op_sel_hi:[1,0]
	v_max_f32_e32 v132, 0, v70
	v_max_f32_e32 v133, 0, v71
	v_max_f32_e32 v134, 0, v72
	v_max_f32_e32 v135, 0, v73
	v_max_f32_e32 v136, 0, v66
	v_max_f32_e32 v137, 0, v67
	v_max_f32_e32 v138, 0, v68
	v_max_f32_e32 v139, 0, v69
	v_pk_mul_f32 v[70:71], v[70:71], v[132:133]
	v_pk_mul_f32 v[72:73], v[72:73], v[134:135]
	v_pk_mul_f32 v[66:67], v[66:67], v[136:137]
	v_pk_mul_f32 v[68:69], v[68:69], v[138:139]
	v_cvt_pk_bf16_f32 v70, v70, v71
	v_cvt_pk_bf16_f32 v71, v72, v73
	v_cvt_pk_bf16_f32 v72, v66, v67
	v_cvt_pk_bf16_f32 v73, v68, v69
	global_store_dwordx4 v[176:177], v[70:73], off offset:256
	s_mov_b64 s[40:41], 0x120000
	v_lshl_add_u64 v[174:175], v[172:173], 0, s[40:41]
	v_pk_mul_f32 v[46:47], v[46:47], v[154:155] op_sel_hi:[1,0]
	v_pk_mul_f32 v[48:49], v[48:49], v[154:155] op_sel_hi:[1,0]
	v_pk_mul_f32 v[42:43], v[42:43], v[154:155] op_sel_hi:[1,0]
	v_pk_mul_f32 v[44:45], v[44:45], v[154:155] op_sel_hi:[1,0]
	v_max_f32_e32 v132, 0, v46
	v_max_f32_e32 v133, 0, v47
	v_max_f32_e32 v134, 0, v48
	v_max_f32_e32 v135, 0, v49
	v_max_f32_e32 v136, 0, v42
	v_max_f32_e32 v137, 0, v43
	v_max_f32_e32 v138, 0, v44
	v_max_f32_e32 v139, 0, v45
	v_pk_mul_f32 v[46:47], v[46:47], v[132:133]
	v_pk_mul_f32 v[48:49], v[48:49], v[134:135]
	v_pk_mul_f32 v[42:43], v[42:43], v[136:137]
	v_pk_mul_f32 v[44:45], v[44:45], v[138:139]
	v_cvt_pk_bf16_f32 v46, v46, v47
	v_cvt_pk_bf16_f32 v47, v48, v49
	v_cvt_pk_bf16_f32 v48, v42, v43
	v_cvt_pk_bf16_f32 v49, v44, v45
	global_store_dwordx4 v[174:175], v[46:49], off
	v_pk_mul_f32 v[38:39], v[38:39], v[154:155] op_sel_hi:[1,0]
	v_pk_mul_f32 v[40:41], v[40:41], v[154:155] op_sel_hi:[1,0]
	v_pk_mul_f32 v[34:35], v[34:35], v[154:155] op_sel_hi:[1,0]
	v_pk_mul_f32 v[36:37], v[36:37], v[154:155] op_sel_hi:[1,0]
	v_max_f32_e32 v132, 0, v38
	v_max_f32_e32 v133, 0, v39
	v_max_f32_e32 v134, 0, v40
	v_max_f32_e32 v135, 0, v41
	v_max_f32_e32 v136, 0, v34
	v_max_f32_e32 v137, 0, v35
	v_max_f32_e32 v138, 0, v36
	v_max_f32_e32 v139, 0, v37
	v_pk_mul_f32 v[38:39], v[38:39], v[132:133]
	v_pk_mul_f32 v[40:41], v[40:41], v[134:135]
	v_pk_mul_f32 v[34:35], v[34:35], v[136:137]
	v_pk_mul_f32 v[36:37], v[36:37], v[138:139]
	v_cvt_pk_bf16_f32 v38, v38, v39
	v_cvt_pk_bf16_f32 v39, v40, v41
	v_cvt_pk_bf16_f32 v40, v34, v35
	v_cvt_pk_bf16_f32 v41, v36, v37
	global_store_dwordx4 v[174:175], v[38:41], off offset:256
	s_mov_b64 s[40:41], 0x160000
	v_lshl_add_u64 v[176:177], v[172:173], 0, s[40:41]
	v_pk_mul_f32 v[14:15], v[14:15], v[194:195] op_sel_hi:[1,0]
	v_pk_mul_f32 v[16:17], v[16:17], v[194:195] op_sel_hi:[1,0]
	v_pk_mul_f32 v[10:11], v[10:11], v[194:195] op_sel_hi:[1,0]
	v_pk_mul_f32 v[12:13], v[12:13], v[194:195] op_sel_hi:[1,0]
	v_max_f32_e32 v132, 0, v14
	v_max_f32_e32 v133, 0, v15
	v_max_f32_e32 v134, 0, v16
	v_max_f32_e32 v135, 0, v17
	v_max_f32_e32 v136, 0, v10
	v_max_f32_e32 v137, 0, v11
	v_max_f32_e32 v138, 0, v12
	v_max_f32_e32 v139, 0, v13
	v_pk_mul_f32 v[14:15], v[14:15], v[132:133]
	v_pk_mul_f32 v[16:17], v[16:17], v[134:135]
	v_pk_mul_f32 v[10:11], v[10:11], v[136:137]
	v_pk_mul_f32 v[12:13], v[12:13], v[138:139]
	v_cvt_pk_bf16_f32 v14, v14, v15
	v_cvt_pk_bf16_f32 v15, v16, v17
	v_cvt_pk_bf16_f32 v16, v10, v11
	v_cvt_pk_bf16_f32 v17, v12, v13
	global_store_dwordx4 v[176:177], v[14:17], off
	v_pk_mul_f32 v[6:7], v[6:7], v[194:195] op_sel_hi:[1,0]
	v_pk_mul_f32 v[8:9], v[8:9], v[194:195] op_sel_hi:[1,0]
	v_pk_mul_f32 v[2:3], v[2:3], v[194:195] op_sel_hi:[1,0]
	v_pk_mul_f32 v[4:5], v[4:5], v[194:195] op_sel_hi:[1,0]
	v_max_f32_e32 v132, 0, v6
	v_max_f32_e32 v133, 0, v7
	v_max_f32_e32 v134, 0, v8
	v_max_f32_e32 v135, 0, v9
	v_max_f32_e32 v136, 0, v2
	v_max_f32_e32 v137, 0, v3
	v_max_f32_e32 v138, 0, v4
	v_max_f32_e32 v139, 0, v5
	v_pk_mul_f32 v[6:7], v[6:7], v[132:133]
	v_pk_mul_f32 v[8:9], v[8:9], v[134:135]
	v_pk_mul_f32 v[2:3], v[2:3], v[136:137]
	v_pk_mul_f32 v[4:5], v[4:5], v[138:139]
	v_cvt_pk_bf16_f32 v6, v6, v7
	v_cvt_pk_bf16_f32 v7, v8, v9
	v_cvt_pk_bf16_f32 v8, v2, v3
	v_cvt_pk_bf16_f32 v9, v4, v5
	global_store_dwordx4 v[176:177], v[6:9], off offset:256
	s_nop 3
	v_mfma_f32_32x32x16_bf16 v[2:17], v[204:207], v[204:207], 0
	v_mfma_f32_32x32x16_bf16 v[18:33], v[204:207], v[204:207], 0
	v_mfma_f32_32x32x16_bf16 v[34:49], v[204:207], v[204:207], 0
	v_mfma_f32_32x32x16_bf16 v[50:65], v[204:207], v[204:207], 0
	v_mfma_f32_32x32x16_bf16 v[66:81], v[204:207], v[204:207], 0
	v_mfma_f32_32x32x16_bf16 v[82:97], v[204:207], v[204:207], 0
	v_mfma_f32_32x32x16_bf16 v[98:113], v[204:207], v[204:207], 0
	v_mfma_f32_32x32x16_bf16 v[114:129], v[204:207], v[204:207], 0
	s_mov_b64 s[6:7], -1
	s_andn2_b64 vcc, exec, s[38:39]
	s_cbranch_vccnz .LBB0_2618
	s_andn2_b64 vcc, exec, s[10:11]
	s_cbranch_vccnz .LBB0_2617
	s_branch .LBB0_2617
